# strength-reduced filler address generation in both attention tile loops (per-lane constant offsets + saddr, slot-linear scalar bases) on top of P11 rewrite
# speedup vs baseline: 1.0084x; 1.0084x over previous
; DEV int ltid() { int t = threadIdx.x; asm volatile("" : "+v"(t)); return t; }
; DEV unsigned cvt_pk_bf16(float lo, float hi) { const f32x2 v = {lo, hi}; const bf16n2 r = __builtin_convertvector(v, bf16n2); return __builtin_bit_cast(unsigned, r); }
; DEV float bf2f(bf16_t v) { return __uint_as_float(((unsigned)v) << 16); }
; DEV int v_st(int k, int c) { const int kk = (k & ~0xC) | ((k & 4) << 1) | ((k & 8) >> 1); return ((kk >> 3) * 4 + (c >> 5)) * 512 + ((kk & 7) * 32 + (c & 31)) * 2; }
; DEV void fill_load(CParams& p, int wg, int slot, f32x4 (&ld)[4]) {
;   const FillDesc d = fill_decode(p, wg, slot); const int tid = ltid(), tx = tid & 15, ty = tid >> 4;
;   const float* sp = d.src + (long)(d.kh + 4 * ty) * d.ldsrc + d.n0 + 4 * tx;
; #pragma unroll
;   for (int r = 0; r < 4; ++r) ld[r] = *(const f32x4*)(sp + (long)r * d.ldsrc);
; DEV void attn_unit(const bf16_t* __restrict__ Qb, const bf16_t* __restrict__ Kh, const bf16_t* __restrict__ Vh, const float* __restrict__ rp, bf16_t* __restrict__ Ob, CParams& fp, int fwg, int fbase, int fn) {
;     ...
; #pragma unroll
;     for (int dd = 0; dd < 2; ++dd) {
;       const int a0 = 16 * dd + 8 * hi;
;       const f32x4 c0 = *(const f32x4*)(rr + a0), c1 = *(const f32x4*)(rr + a0 + 4), s0 = *(const f32x4*)(rr + 32 + a0), s1 = *(const f32x4*)(rr + 32 + a0 + 4);
;       float cs[8] = {c0[0], c0[1], c0[2], c0[3], c1[0], c1[1], c1[2], c1[3]}, sn[8] = {s0[0], s0[1], s0[2], s0[3], s1[0], s1[1], s1[2], s1[3]};
;       const bf16x8 x1 = qr[8 + dd], x2 = qr[10 + dd]; bf16x8 y1, y2;
; #pragma unroll
;       for (int j = 0; j < 8; j += 2) {
;         const float a1 = bf2f((bf16_t)x1[j]), a2 = bf2f((bf16_t)x2[j]), b1 = bf2f((bf16_t)x1[j + 1]), b2 = bf2f((bf16_t)x2[j + 1]);
;         const unsigned u1 = cvt_pk_bf16(a1 * cs[j] - a2 * sn[j], b1 * cs[j + 1] - b2 * sn[j + 1]);
;         const unsigned u2 = cvt_pk_bf16(a1 * sn[j] + a2 * cs[j], b1 * sn[j + 1] + b2 * cs[j + 1]);
;         y1[j] = (short)(u1 & 0xffff); y1[j + 1] = (short)(u1 >> 16); y2[j] = (short)(u2 & 0xffff); y2[j + 1] = (short)(u2 >> 16);
;       }
;       qr[8 + dd] = y1; qr[10 + dd] = y2;
;     }
;   }
;   const int sr = tid >> 4, sc = (tid & 15) * 8, vst0 = v_st(sr, sc), vst1 = v_st(32 + sr, sc);
;   int kst[3];
; #pragma unroll
;   for (int i = 0; i < 3; ++i) { const int id = tid + 512 * i, row = id / 24, ch = id % 24; kst[i] = KSWZ2(row, ch * 16); }
.LBB0_890:
	s_waitcnt vmcnt(11)
	v_and_b32_e32 v83, 0xffff0000, v58
	v_lshlrev_b32_e32 v82, 16, v58
	s_waitcnt vmcnt(9)
	v_and_b32_e32 v85, 0xffff0000, v50
	v_lshlrev_b32_e32 v84, 16, v50
	s_waitcnt vmcnt(4)
	v_pk_mul_f32 v[86:87], v[66:67], v[84:85]
	v_pk_mul_f32 v[66:67], v[66:67], v[82:83]
	v_pk_fma_f32 v[86:87], v[62:63], v[82:83], v[86:87] neg_lo:[0,0,1] neg_hi:[0,0,1]
	v_pk_fma_f32 v[62:63], v[62:63], v[84:85], v[66:67]
	v_lshlrev_b32_e32 v58, 16, v51
	v_cvt_pk_bf16_f32 v136, v62, v63
	v_and_b32_e32 v63, 0xffff0000, v59
	v_lshlrev_b32_e32 v62, 16, v59
	v_and_b32_e32 v59, 0xffff0000, v51
	v_pk_mul_f32 v[50:51], v[68:69], v[58:59]
	s_mov_b32 s21, 0x2aaaaaab
	v_pk_fma_f32 v[50:51], v[64:65], v[62:63], v[50:51] neg_lo:[0,0,1] neg_hi:[0,0,1]
	s_lshl_b32 s19, s20, s19
	v_cvt_pk_bf16_f32 v133, v50, v51
	v_pk_mul_f32 v[50:51], v[68:69], v[62:63]
	s_and_b32 s19, s19, 0x780
	v_pk_fma_f32 v[50:51], v[64:65], v[58:59], v[50:51]
	v_and_b32_e32 v59, 0xffff0000, v52
	v_lshlrev_b32_e32 v58, 16, v52
	v_cvt_pk_bf16_f32 v137, v50, v51
	v_and_b32_e32 v51, 0xffff0000, v60
	v_lshlrev_b32_e32 v50, 16, v60
	v_pk_mul_f32 v[62:63], v[54:55], v[58:59]
	s_mov_b32 s17, 0
	v_pk_fma_f32 v[62:63], v[46:47], v[50:51], v[62:63] neg_lo:[0,0,1] neg_hi:[0,0,1]
	v_pk_mul_f32 v[50:51], v[54:55], v[50:51]
	v_mov_b32_e32 v67, 0
	v_pk_fma_f32 v[46:47], v[46:47], v[58:59], v[50:51]
	v_and_b32_e32 v51, 0xffff0000, v53
	v_lshlrev_b32_e32 v50, 16, v53
	v_cvt_pk_bf16_f32 v138, v46, v47
	v_and_b32_e32 v47, 0xffff0000, v61
	v_lshlrev_b32_e32 v46, 16, v61
	v_pk_mul_f32 v[52:53], v[56:57], v[50:51]
	v_and_b32_e32 v77, 0x3fffffc0, v1
	v_pk_fma_f32 v[52:53], v[48:49], v[46:47], v[52:53] neg_lo:[0,0,1] neg_hi:[0,0,1]
	v_pk_mul_f32 v[46:47], v[56:57], v[46:47]
	s_add_i32 s77, 0, 0x18000
	v_pk_fma_f32 v[46:47], v[48:49], v[50:51], v[46:47]
	v_and_b32_e32 v49, 0xffff0000, v22
	v_cvt_pk_bf16_f32 v139, v46, v47
	v_and_b32_e32 v47, 0xffff0000, v30
	v_lshlrev_b32_e32 v46, 16, v30
	v_lshlrev_b32_e32 v48, 16, v22
	s_waitcnt vmcnt(0)
	v_pk_mul_f32 v[50:51], v[42:43], v[48:49]
	v_pk_mul_f32 v[42:43], v[42:43], v[46:47]
	v_pk_fma_f32 v[50:51], v[38:39], v[46:47], v[50:51] neg_lo:[0,0,1] neg_hi:[0,0,1]
	v_pk_fma_f32 v[38:39], v[38:39], v[48:49], v[42:43]
	v_lshlrev_b32_e32 v30, 16, v23
	v_cvt_pk_bf16_f32 v144, v38, v39
	v_and_b32_e32 v39, 0xffff0000, v31
	v_lshlrev_b32_e32 v38, 16, v31
	v_and_b32_e32 v31, 0xffff0000, v23
	v_pk_mul_f32 v[22:23], v[44:45], v[30:31]
	v_lshl_add_u32 v185, v77, 2, s77
	v_pk_fma_f32 v[22:23], v[40:41], v[38:39], v[22:23] neg_lo:[0,0,1] neg_hi:[0,0,1]
	v_mov_b32_e32 v77, v67
	v_cvt_pk_bf16_f32 v141, v22, v23
	v_pk_mul_f32 v[22:23], v[44:45], v[38:39]
	s_movk_i32 s28, 0xc0
	v_pk_fma_f32 v[22:23], v[40:41], v[30:31], v[22:23]
	v_and_b32_e32 v31, 0xffff0000, v24
	v_lshlrev_b32_e32 v30, 16, v24
	v_cvt_pk_bf16_f32 v145, v22, v23
	v_and_b32_e32 v23, 0xffff0000, v32
	v_lshlrev_b32_e32 v22, 16, v32
	v_pk_mul_f32 v[38:39], v[34:35], v[30:31]
	v_cvt_pk_bf16_f32 v134, v62, v63
	v_pk_fma_f32 v[38:39], v[26:27], v[22:23], v[38:39] neg_lo:[0,0,1] neg_hi:[0,0,1]
	v_pk_mul_f32 v[22:23], v[34:35], v[22:23]
	v_cvt_pk_bf16_f32 v135, v52, v53
	v_pk_fma_f32 v[22:23], v[26:27], v[30:31], v[22:23]
	v_and_b32_e32 v27, 0xffff0000, v25
	v_lshlrev_b32_e32 v26, 16, v25
	v_cvt_pk_bf16_f32 v146, v22, v23
	v_and_b32_e32 v23, 0xffff0000, v33
	v_lshlrev_b32_e32 v22, 16, v33
	v_pk_mul_f32 v[24:25], v[36:37], v[26:27]
	v_cvt_pk_bf16_f32 v140, v50, v51
	v_pk_fma_f32 v[24:25], v[28:29], v[22:23], v[24:25] neg_lo:[0,0,1] neg_hi:[0,0,1]
	v_pk_mul_f32 v[22:23], v[36:37], v[22:23]
	v_cvt_pk_bf16_f32 v143, v24, v25
	v_pk_fma_f32 v[22:23], v[28:29], v[26:27], v[22:23]
	v_and_b32_e32 v25, 3, v74
	v_cvt_pk_bf16_f32 v147, v22, v23
	v_and_b32_e32 v22, 0xfffff0, v74
	v_lshlrev_b32_e32 v23, 1, v74
	v_and_or_b32 v22, v23, 8, v22
	v_lshrrev_b32_e32 v23, 1, v74
	v_and_or_b32 v23, v23, 4, v25
	v_and_b32_e32 v25, 0xfffff0, v78
	v_lshlrev_b32_e32 v26, 1, v78
	v_and_or_b32 v25, v26, 8, v25
	v_lshrrev_b32_e32 v22, 1, v22
	v_lshrrev_b32_e32 v24, 5, v80
	v_lshrrev_b32_e32 v25, 1, v25
	v_or_b32_e32 v22, v22, v24
	v_or_b32_e32 v24, v25, v24
	v_mul_hi_i32 v25, v1, s21
	v_lshrrev_b32_e32 v26, 31, v25
	v_ashrrev_i32_e32 v25, 2, v25
	v_add_u32_e32 v25, v25, v26
	v_mul_lo_u32 v26, v25, 24
	v_sub_u32_e32 v26, v1, v26
	v_lshlrev_b32_e32 v27, 9, v25
	v_bitop3_b32 v25, v25, v26, 15 bitop3:0x6c
	v_lshl_add_u32 v195, v25, 4, v27
	v_add_u32_e32 v25, 0x200, v1
	v_mul_hi_i32 v26, v25, s21
	v_lshrrev_b32_e32 v27, 31, v26
	v_ashrrev_i32_e32 v26, 2, v26
	v_add_u32_e32 v26, v26, v27
	v_mul_lo_u32 v27, v26, 24
	v_sub_u32_e32 v25, v25, v27
	v_lshlrev_b32_e32 v27, 9, v26
	v_bitop3_b32 v25, v26, v25, 15 bitop3:0x6c
	v_lshl_add_u32 v196, v25, 4, v27
	v_add_u32_e32 v25, 0x400, v1
	v_mul_hi_i32 v26, v25, s21
	v_lshrrev_b32_e32 v27, 31, v26
	v_ashrrev_i32_e32 v26, 2, v26
	v_add_u32_e32 v26, v26, v27
	v_mul_lo_u32 v27, v26, 24
	v_sub_u32_e32 v25, v25, v27
	v_lshlrev_b32_e32 v27, 9, v26
	v_bitop3_b32 v25, v26, v25, 15 bitop3:0x6c
	v_lshlrev_b32_e32 v22, 9, v22
	v_lshlrev_b32_e32 v23, 6, v23
	v_lshl_add_u32 v197, v25, 4, v27
	v_and_b32_e32 v25, 48, v76
	v_lshlrev_b32_e32 v24, 9, v24
	v_or3_b32 v198, v22, v23, v25
	v_lshlrev_b32_e32 v22, 4, v187
	v_or3_b32 v199, v24, v23, v25
	v_and_b32_e32 v27, 0xc0, v22
	v_lshlrev_b32_e32 v22, 1, v187
	v_mov_b32_e32 v24, v0
	v_and_b32_e32 v28, 32, v22
	s_lshl_b32 s21, s2, 6
	s_and_b32 s53, s21, 64
	v_ashrrev_i32_e32 v22, 2, v24
	s_lshl_b32 s21, s20, 7
	v_and_b32_e32 v22, -4, v22
	s_and_b32 s16, s16, s21
	v_add_u32_e32 v22, s19, v22
	s_or_b32 s16, s16, s53
	v_mad_i64_i32 v[22:23], s[20:21], s18, v22, 0
; DEV FillDesc fill_decode(CParams& p, int wg, int slot) {
;   const int h = slot * 256 + wg, t = h >> 1, half = h & 1; FillDesc d;
;   if (t < NE * 512) { const int e = t >> 9, r = t & 511; d.src = p.w_gu + (long)e * 2048 * 4096; d.ldsrc = 4096; d.dst = p.wt_gu8 + (long)e * 4096 * 2048; d.perm = 2; d.n0 = (r & 31) * 128 + 64 * half; d.kh = (r >> 5) * 128; }
;   else { const int v = t - NE * 512, e = v >> 8, r = v & 255; d.src = p.w_dn + (long)e * 2048 * 2048; d.ldsrc = 2048; d.dst = p.wt_dn8 + (long)e * 2048 * 2048; d.perm = 0; d.n0 = (r & 15) * 128 + 64 * half; d.kh = (r >> 4) * 128; }
;   return d;
; }
; DEV void fill_load(CParams& p, int wg, int slot, f32x4 (&ld)[4]) {
;   const FillDesc d = fill_decode(p, wg, slot); const int tid = ltid(), tx = tid & 15, ty = tid >> 4;
;   const float* sp = d.src + (long)(d.kh + 4 * ty) * d.ldsrc + d.n0 + 4 * tx;
; #pragma unroll
;   for (int r = 0; r < 4; ++r) ld[r] = *(const f32x4*)(sp + (long)r * d.ldsrc);
; }
; DEV void fill_write(const f32x4 (&ld)[4], int bufsel) {
;   extern __shared__ __attribute__((aligned(16))) char shm[];
;   unsigned* T = (unsigned*)(shm + FILL_LDS_OFF + bufsel * FILL_TB); const int tid = ltid(), tx = tid & 15, ty = tid >> 4;
;   constexpr float WS = (float)(1 << FP8_WSCALE_LOG2_);
; #pragma unroll
;   for (int j = 0; j < 4; ++j) T[(4 * tx + j) * 33 + ty] = cvt_pk4_fp8((f32x4){ld[0][j] * WS, ld[1][j] * WS, ld[2][j] * WS, ld[3][j] * WS});
; }
; DEV void fill_store(CParams& p, int wg, int slot, int bufsel) {
;   extern __shared__ __attribute__((aligned(16))) char shm[];
;   const unsigned* T = (const unsigned*)(shm + FILL_LDS_OFF + bufsel * FILL_TB); const int tid = ltid(), nl = tid >> 3, cc = tid & 7;
;   const FillDesc d = fill_decode(p, wg, slot);
;   u32x4 v; v.x = T[nl * 33 + 4 * cc]; v.y = T[nl * 33 + 4 * cc + 1]; v.z = T[nl * 33 + 4 * cc + 2]; v.w = T[nl * 33 + 4 * cc + 3];
;   *(u32x4*)(d.dst + (long)perm_row(d.perm, d.n0 + nl) * 2048 + d.kh + 16 * cc) = v;
; DEV void attn_unit(const bf16_t* __restrict__ Qb, const bf16_t* __restrict__ Kh, const bf16_t* __restrict__ Vh, const float* __restrict__ rp, bf16_t* __restrict__ Ob, CParams& fp, int fwg, int fbase, int fn) {
;     ...
;   f32x16 p0, p1; float mn, al; bf16x8 pa0, pa1, pa2, pa3; constexpr int NTL = KEYS / KVBLK;
;   f32x4 fld[4];
;   if (fn > 0) fill_load(fp, fwg, fbase, fld);
;   SWRITE(0); SLOAD(KVBLK); __syncthreads();
	v_lshl_add_u64 v[22:23], v[22:23], 2, s[14:15]
	s_lshl_b32 s16, s16, 2
	v_lshlrev_b32_e32 v24, 4, v24
	v_lshl_add_u64 v[22:23], v[22:23], 0, s[16:17]
	v_and_b32_e32 v66, 0xf0, v24
	v_lshl_add_u64 v[22:23], v[22:23], 0, v[66:67]
	s_lshl_b32 s16, s18, 2
	v_lshl_add_u64 v[24:25], v[22:23], 0, s[16:17]
	global_load_dwordx4 v[168:171], v[22:23], off
	global_load_dwordx4 v[172:175], v[24:25], off
	v_lshl_add_u64 v[22:23], v[24:25], 0, s[16:17]
	v_lshl_add_u64 v[24:25], v[22:23], 0, s[16:17]
	global_load_dwordx4 v[176:179], v[22:23], off
	global_load_dwordx4 v[180:183], v[24:25], off
	v_add_u32_e32 v22, 0, v198
	ds_write_b128 v22, v[6:9]
	v_add_u32_e32 v6, 0, v199
	ds_write_b128 v6, v[2:5]
	v_add_u32_e32 v2, 0, v195
	ds_write_b128 v2, v[10:13] offset:32768
	v_add_u32_e32 v2, 0, v196
	ds_write_b128 v2, v[14:17] offset:32768
	v_add_u32_e32 v2, 0, v197
	ds_write_b128 v2, v[18:21] offset:32768
	v_lshlrev_b64 v[2:3], 8, v[74:75]
	v_lshl_add_u64 v[2:3], s[12:13], 0, v[2:3]
	v_lshl_add_u64 v[2:3], v[2:3], 0, v[76:77]
	s_movk_i32 s12, 0x4000
	v_add_co_u32_e32 v4, vcc, s12, v2
	s_movk_i32 s12, 0x6000
	s_nop 0
	v_addc_co_u32_e32 v5, vcc, 0, v3, vcc
	v_add_co_u32_e32 v2, vcc, s12, v2
	v_lshlrev_b32_e32 v26, 3, v187
	s_nop 0
	v_addc_co_u32_e32 v3, vcc, 0, v3, vcc
	global_load_dwordx4 v[148:151], v[4:5], off
	global_load_dwordx4 v[152:155], v[2:3], off
	v_lshlrev_b64 v[2:3], 1, v[72:73]
	v_lshl_add_u64 v[4:5], s[4:5], 0, v[2:3]
	v_add_co_u32_e32 v6, vcc, s12, v4
	s_mov_b32 s4, 0x8000
	s_nop 0
	v_addc_co_u32_e32 v7, vcc, 0, v5, vcc
	v_add_co_u32_e32 v8, vcc, s4, v4
	s_mov_b32 s4, 0xa000
	s_nop 0
	v_addc_co_u32_e32 v9, vcc, 0, v5, vcc
	v_add_co_u32_e32 v4, vcc, s4, v4
	global_load_dwordx4 v[156:159], v[6:7], off
	global_load_dwordx4 v[160:163], v[8:9], off
	v_addc_co_u32_e32 v5, vcc, 0, v5, vcc
	global_load_dwordx4 v[164:167], v[4:5], off
	v_lshlrev_b32_e32 v4, 4, v192
	v_and_b32_e32 v5, 0xf0, v4
	s_movk_i32 s4, 0x60
	v_bitop3_b32 v204, v186, v5, s4 bitop3:0x36
	s_movk_i32 s4, 0x80
	v_bitop3_b32 v205, v186, v5, s4 bitop3:0x36
	s_movk_i32 s4, 0xa0
	v_bitop3_b32 v206, v186, v5, s4 bitop3:0x36
	s_movk_i32 s4, 0xe0
	v_bitop3_b32 v208, v186, v5, s4 bitop3:0x36
	s_movk_i32 s4, 0x100
	v_bitop3_b32 v209, v186, v5, s4 bitop3:0x36
	s_movk_i32 s4, 0x120
	s_movk_i32 s19, 0xf0
	v_bitop3_b32 v211, v186, v5, s4 bitop3:0x36
	s_movk_i32 s4, 0x140
	s_movk_i32 s16, 0x118
	s_cmp_lg_u32 0, -1
	v_bitop3_b32 v201, v186, v4, s19 bitop3:0x78
	v_bitop3_b32 v212, v186, v5, s4 bitop3:0x36
	s_movk_i32 s4, 0x160
	v_and_or_b32 v4, v26, s16, v28
	s_cselect_b32 s16, 0, 0
	v_and_b32_e32 v6, 15, v1
	s_waitcnt lgkmcnt(0)
	s_barrier
	s_load_dwordx4 s[12:15], s[22:23], 0xe8
	v_bitop3_b32 v202, v186, v5, 32 bitop3:0x36
	v_bitop3_b32 v203, v186, v5, 64 bitop3:0x36
	v_bitop3_b32 v207, v186, v5, s28 bitop3:0x36
	v_bitop3_b32 v213, v186, v5, s4 bitop3:0x36
	s_load_dwordx2 s[18:19], s[22:23], 0xa0
	s_load_dwordx2 s[20:21], s[22:23], 0xb0
	v_add3_u32 v214, v27, s16, v4
	v_lshl_add_u64 v[4:5], s[24:25], 0, v[70:71]
	v_lshlrev_b32_e32 v66, 4, v6
	s_add_u32 s6, s6, s27
	v_lshl_add_u64 v[4:5], v[4:5], 0, v[66:67]
	s_addc_u32 s7, s7, s26
	v_lshl_add_u64 v[4:5], s[8:9], 0, v[4:5]
	s_mov_b64 s[8:9], 0xa000
	v_lshl_add_u64 v[2:3], s[6:7], 0, v[2:3]
	s_mov_b64 s[6:7], 0x10000
	v_mov_b32_e32 v66, v67
	v_cvt_pk_bf16_f32 v142, v38, v39
	v_lshl_add_u64 v[188:189], v[4:5], 0, s[8:9]
	v_lshl_add_u64 v[190:191], v[2:3], 0, s[6:7]
	v_mov_b32_e32 v68, v67
	v_mov_b32_e32 v69, v67
	v_mov_b32_e32 v70, v67
	v_mov_b32_e32 v71, v67
	v_mov_b32_e32 v72, v67
	v_mov_b32_e32 v73, v67
	v_mov_b32_e32 v74, v67
	v_mov_b32_e32 v75, v67
	v_mov_b32_e32 v76, v67
	v_mov_b32_e32 v78, v67
	v_mov_b32_e32 v79, v67
	v_mov_b32_e32 v80, v67
	v_mov_b32_e32 v81, v67
	v_mov_b64_e32 v[50:51], v[66:67]
	v_mov_b64_e32 v[34:35], v[66:67]
	v_mov_b64_e32 v[18:19], v[66:67]
	v_mov_b64_e32 v[2:3], v[66:67]
	v_cvt_pk_bf16_f32 v132, v86, v87
	v_lshlrev_b32_e32 v200, 9, v192
	v_cmp_gt_u32_e64 s[4:5], 32, v187
	v_lshl_add_u32 v210, v192, 2, v185
	v_mov_b32_e32 v215, 0xf149f2ca
	s_movk_i32 s28, 0xbc00
	s_mov_b32 s34, -2
	s_movk_i32 s29, 0x84
	s_movk_i32 s30, 0x7ff
	s_mov_b32 s31, 0x42ddb3d8
	s_mov_b64 s[8:9], 0x4000
	s_mov_b64 s[22:23], 0x6000
	v_mov_b32_e32 v216, 0xfffff800
	v_mov_b32_e32 v217, 0x80
	v_mov_b64_e32 v[52:53], v[68:69]
	v_mov_b64_e32 v[54:55], v[70:71]
	v_mov_b64_e32 v[56:57], v[72:73]
	v_mov_b64_e32 v[58:59], v[74:75]
	v_mov_b64_e32 v[60:61], v[76:77]
	v_mov_b64_e32 v[62:63], v[78:79]
	v_mov_b64_e32 v[64:65], v[80:81]
	v_mov_b64_e32 v[36:37], v[68:69]
	v_mov_b64_e32 v[38:39], v[70:71]
	v_mov_b64_e32 v[40:41], v[72:73]
	v_mov_b64_e32 v[42:43], v[74:75]
	v_mov_b64_e32 v[44:45], v[76:77]
	v_mov_b64_e32 v[46:47], v[78:79]
	v_mov_b64_e32 v[48:49], v[80:81]
	v_mov_b64_e32 v[20:21], v[68:69]
	v_mov_b64_e32 v[22:23], v[70:71]
	v_mov_b64_e32 v[24:25], v[72:73]
	v_mov_b64_e32 v[26:27], v[74:75]
	v_mov_b64_e32 v[28:29], v[76:77]
	v_mov_b64_e32 v[30:31], v[78:79]
	v_mov_b64_e32 v[32:33], v[80:81]
	v_mov_b64_e32 v[4:5], v[68:69]
	v_mov_b64_e32 v[6:7], v[70:71]
	v_mov_b64_e32 v[8:9], v[72:73]
	v_mov_b64_e32 v[10:11], v[74:75]
	v_mov_b64_e32 v[12:13], v[76:77]
	v_mov_b64_e32 v[14:15], v[78:79]
	v_mov_b64_e32 v[16:17], v[80:81]
	v_mov_b32_e32 v218, 0
	s_waitcnt lgkmcnt(0)
	s_lshr_b32 s56, s2, 1
	s_and_b32 s57, s56, 31
	s_lshl_b32 s57, s57, 7
	s_or_b32 s57, s57, s53
	s_lshr_b32 s58, s56, 5
	s_lshl_b32 s58, s58, 7
	s_and_b32 s59, s56, 15
	s_lshl_b32 s59, s59, 7
	s_or_b32 s59, s59, s53
	s_lshr_b32 s60, s56, 4
	s_lshl_b32 s60, s60, 7
	v_lshrrev_b32_e32 v253, 3, v0
	v_and_b32_e32 v254, 7, v0
	v_lshlrev_b32_e32 v254, 4, v254
	v_mul_u32_u24_e32 v244, 0x84, v253
	v_add_u32_e32 v244, v244, v254
	v_add_u32_e32 v244, 0x20800, v244
	v_and_b32_e32 v255, 15, v0
	v_mul_u32_u24_e32 v245, 0x210, v255
	v_lshrrev_b32_e32 v252, 4, v0
	v_lshl_add_u32 v245, v252, 2, v245
	v_add_u32_e32 v245, 0x20800, v245
	v_add_u32_e32 v246, s57, v253
	v_and_b32_e32 v247, 0x7ff, v246
	v_lshrrev_b32_e32 v246, 11, v246
	v_lshlrev_b32_e32 v246, 7, v246
	v_and_b32_e32 v251, 0x7f, v247
	v_or_b32_e32 v246, v246, v251
	v_lshrrev_b32_e32 v247, 7, v247
	v_lshl_or_b32 v246, v247, 8, v246
	v_lshlrev_b32_e32 v246, 11, v246
	v_add_u32_e32 v246, v246, v254
	v_add_u32_e32 v246, s58, v246
	v_add_u32_e32 v247, s59, v253
	v_lshlrev_b32_e32 v247, 11, v247
	v_add_u32_e32 v247, v247, v254
	v_add_u32_e32 v247, s60, v247
	v_lshlrev_b32_e32 v251, 2, v252
	v_lshlrev_b32_e32 v255, 2, v255
	v_add_u32_e32 v248, s58, v251
	v_lshlrev_b32_e32 v248, 14, v248
	v_add_u32_e32 v249, s57, v255
	v_lshl_add_u32 v248, v249, 2, v248
	v_add_u32_e32 v252, s60, v251
	v_lshlrev_b32_e32 v252, 13, v252
	v_add_u32_e32 v249, s59, v255
	v_lshl_add_u32 v252, v249, 2, v252
	v_add_u32_e32 v249, 0x4000, v248
	v_add_u32_e32 v250, 0x8000, v248
	v_add_u32_e32 v251, 0xc000, v248
	s_add_u32 s62, s18, 0x22000000
	s_addc_u32 s63, s19, 0
	s_add_i32 s37, s34, 2
	s_and_b32 s36, s37, 1
	s_cmpk_eq_i32 s34, 0x41
	s_cbranch_scc0 .LBB0_893

; DEV void fill_store(CParams& p, int wg, int slot, int bufsel) {
;   extern __shared__ __attribute__((aligned(16))) char shm[];
;   const unsigned* T = (const unsigned*)(shm + FILL_LDS_OFF + bufsel * FILL_TB); const int tid = ltid(), nl = tid >> 3, cc = tid & 7;
;   const FillDesc d = fill_decode(p, wg, slot);
;   u32x4 v; v.x = T[nl * 33 + 4 * cc]; v.y = T[nl * 33 + 4 * cc + 1]; v.z = T[nl * 33 + 4 * cc + 2]; v.w = T[nl * 33 + 4 * cc + 3];
;   *(u32x4*)(d.dst + (long)perm_row(d.perm, d.n0 + nl) * 2048 + d.kh + 16 * cc) = v;
; }
; DEV void partialSM(f32x16& p0, f32x16& p1, float& m_reg, float& mn, float& alpha) {
;   constexpr float C = SCALE * 1.4426950408889634f;
;   float pmax = p0[0];
; #pragma unroll
;   for (int r = 1; r < 16; ++r) pmax = fmaxf(pmax, p0[r]);
; #pragma unroll
;   for (int r = 0; r < 16; ++r) pmax = fmaxf(pmax, p1[r]);
;   { auto rr = __builtin_amdgcn_permlane32_swap(__float_as_uint(pmax), __float_as_uint(pmax), false, false);
;     pmax = fmaxf(__uint_as_float(rr[0]), __uint_as_float(rr[1])); }
;   if (__builtin_expect(__all(pmax - m_reg <= THR / SCALE), 1)) { mn = m_reg; alpha = 1.f; }
;   else { mn = fmaxf(m_reg, pmax); alpha = __builtin_amdgcn_exp2f((m_reg - mn) * C); m_reg = mn; }
;   const float mnC = -mn * C;
; #pragma unroll
;   for (int r = 0; r < 16; ++r) p0[r] = fmaf(p0[r], C, mnC);
; #pragma unroll
;   for (int r = 0; r < 16; ++r) p1[r] = fmaf(p1[r], C, mnC);
; #pragma unroll
;   for (int r = 0; r < 16; ++r) p0[r] = __builtin_amdgcn_exp2f(p0[r]);
; }
; DEV void finishSM(f32x16& p0, f32x16& p1, float alpha, float& l_reg, bf16x8& pa0, bf16x8& pa1, bf16x8& pa2, bf16x8& pa3) {
; #pragma unroll
;   for (int r = 0; r < 16; ++r) p1[r] = __builtin_amdgcn_exp2f(p1[r]);
;   float ps = 0;
; #pragma unroll
;   for (int r = 0; r < 16; ++r) ps += p0[r];
; #pragma unroll
;   for (int r = 0; r < 16; ++r) ps += p1[r];
;   { auto rr = __builtin_amdgcn_permlane32_swap(__float_as_uint(ps), __float_as_uint(ps), false, false);
;     ps = __uint_as_float(rr[0]) + __uint_as_float(rr[1]); }
;   l_reg = l_reg * alpha + ps;
;     ...
;   PK4(p0, 0, pa0); PK4(p0, 8, pa1); PK4(p1, 0, pa2); PK4(p1, 8, pa3);
;     ...
; }
; DEV void qkt(f32x16& p0, f32x16& p1, const char* Ks, const bf16x8* qr, int r32, int hi) {
;   p0 = f32x16{}; p1 = f32x16{};
;   __builtin_amdgcn_s_setprio(1);
; #pragma unroll
;   for (int d0 = 0; d0 < 12; ++d0) { const int cb = (d0 * 16 + hi * 8) * 2;
.LBB0_899:
	s_xor_b32 s56, s36, 1
	s_mul_i32 s56, s56, 0x2200
	v_add_u32_e32 v72, s56, v244
	ds_read2_b32 v[68:69], v72 offset1:1
	ds_read2_b32 v[70:71], v72 offset0:2 offset1:3
	s_add_i32 s57, s37, 66
	s_cmp_gt_u32 s57, 0x7f
	s_cbranch_scc1 .Lfst_a_d
	s_lshr_b32 s58, s57, 2
	s_lshl_b32 s58, s58, 23
	s_and_b32 s59, s57, 3
	s_lshl_b32 s59, s59, 9
	s_or_b32 s58, s58, s59
	s_add_u32 s60, s12, s58
	s_addc_u32 s61, s13, 0
	s_waitcnt lgkmcnt(0)
	global_store_dwordx4 v246, v[68:71], s[60:61]
	s_branch .Lfst_a_end
.Lfst_a_d:
	s_sub_u32 s57, s57, 0x80
	s_lshr_b32 s58, s57, 1
	s_lshl_b32 s58, s58, 22
	s_and_b32 s59, s57, 1
	s_lshl_b32 s59, s59, 10
	s_or_b32 s58, s58, s59
	s_add_u32 s60, s14, s58
	s_addc_u32 s61, s15, 0
	s_waitcnt lgkmcnt(0)
	global_store_dwordx4 v247, v[68:71], s[60:61]
.Lfst_a_end:
.LBB0_907:
	s_lshl_b32 s6, s36, 15
	s_add_i32 s6, s6, 0
	s_setprio 1
	v_add3_u32 v66, s6, v201, v200
	ds_read_b128 v[68:71], v66 offset:32768
	ds_read_b128 v[72:75], v66 offset:49152
	v_add3_u32 v66, s6, v202, v200
	ds_read_b128 v[224:227], v66 offset:32768
	ds_read_b128 v[228:231], v66 offset:49152
	v_add3_u32 v66, s6, v203, v200
	s_waitcnt lgkmcnt(0)
	v_mfma_f32_32x32x16_bf16 v[84:99], v[68:71], v[100:103], 0
	v_mfma_f32_32x32x16_bf16 v[68:83], v[72:75], v[100:103], 0
	v_mfma_f32_32x32x16_bf16 v[84:99], v[224:227], v[104:107], v[84:99]
	v_mfma_f32_32x32x16_bf16 v[68:83], v[228:231], v[104:107], v[68:83]
	ds_read_b128 v[224:227], v66 offset:32768
	ds_read_b128 v[228:231], v66 offset:49152
	v_add3_u32 v66, s6, v204, v200
	s_waitcnt lgkmcnt(1)
	v_mfma_f32_32x32x16_bf16 v[84:99], v[224:227], v[108:111], v[84:99]
	s_waitcnt lgkmcnt(0)
	v_mfma_f32_32x32x16_bf16 v[68:83], v[228:231], v[108:111], v[68:83]
	ds_read_b128 v[224:227], v66 offset:32768
	ds_read_b128 v[228:231], v66 offset:49152
	v_add3_u32 v66, s6, v205, v200
	s_waitcnt lgkmcnt(1)
	v_mfma_f32_32x32x16_bf16 v[84:99], v[224:227], v[112:115], v[84:99]
	s_waitcnt lgkmcnt(0)
	v_mfma_f32_32x32x16_bf16 v[68:83], v[228:231], v[112:115], v[68:83]
	ds_read_b128 v[224:227], v66 offset:32768
	ds_read_b128 v[228:231], v66 offset:49152
	v_add3_u32 v66, s6, v206, v200
	s_waitcnt lgkmcnt(1)
	v_mfma_f32_32x32x16_bf16 v[84:99], v[224:227], v[116:119], v[84:99]
	s_waitcnt lgkmcnt(0)
	v_mfma_f32_32x32x16_bf16 v[68:83], v[228:231], v[116:119], v[68:83]
	ds_read_b128 v[224:227], v66 offset:32768
	ds_read_b128 v[228:231], v66 offset:49152
	v_add3_u32 v66, s6, v207, v200
	s_waitcnt lgkmcnt(1)
	v_mfma_f32_32x32x16_bf16 v[84:99], v[224:227], v[120:123], v[84:99]
	s_waitcnt lgkmcnt(0)
	v_mfma_f32_32x32x16_bf16 v[68:83], v[228:231], v[120:123], v[68:83]
	ds_read_b128 v[224:227], v66 offset:32768
	ds_read_b128 v[228:231], v66 offset:49152
	v_add3_u32 v66, s6, v208, v200
	s_waitcnt lgkmcnt(1)
	v_mfma_f32_32x32x16_bf16 v[84:99], v[224:227], v[124:127], v[84:99]
	s_waitcnt lgkmcnt(0)
	v_mfma_f32_32x32x16_bf16 v[68:83], v[228:231], v[124:127], v[68:83]
	ds_read_b128 v[224:227], v66 offset:32768
	ds_read_b128 v[228:231], v66 offset:49152
	v_add3_u32 v66, s6, v209, v200
	s_waitcnt lgkmcnt(1)
	v_mfma_f32_32x32x16_bf16 v[84:99], v[224:227], v[128:131], v[84:99]
	s_waitcnt lgkmcnt(0)
	v_mfma_f32_32x32x16_bf16 v[68:83], v[228:231], v[128:131], v[68:83]
	ds_read_b128 v[224:227], v66 offset:32768
	ds_read_b128 v[228:231], v66 offset:49152
	v_add3_u32 v66, s6, v211, v200
	s_waitcnt lgkmcnt(1)
	v_mfma_f32_32x32x16_bf16 v[84:99], v[224:227], v[132:135], v[84:99]
	s_waitcnt lgkmcnt(0)
	v_mfma_f32_32x32x16_bf16 v[68:83], v[228:231], v[132:135], v[68:83]
	ds_read_b128 v[224:227], v66 offset:32768
	ds_read_b128 v[228:231], v66 offset:49152
	v_add3_u32 v66, s6, v212, v200
	s_waitcnt lgkmcnt(1)
	v_mfma_f32_32x32x16_bf16 v[84:99], v[224:227], v[140:143], v[84:99]
	s_waitcnt lgkmcnt(0)
	v_mfma_f32_32x32x16_bf16 v[68:83], v[228:231], v[140:143], v[68:83]
	ds_read_b128 v[224:227], v66 offset:32768
	ds_read_b128 v[228:231], v66 offset:49152
	v_add3_u32 v66, s6, v213, v200
	s_waitcnt lgkmcnt(1)
	v_mfma_f32_32x32x16_bf16 v[84:99], v[224:227], v[136:139], v[84:99]
	s_waitcnt lgkmcnt(0)
	v_mfma_f32_32x32x16_bf16 v[68:83], v[228:231], v[136:139], v[68:83]
	ds_read_b128 v[224:227], v66 offset:32768
	ds_read_b128 v[228:231], v66 offset:49152
	s_waitcnt lgkmcnt(1)
	v_mfma_f32_32x32x16_bf16 v[84:99], v[224:227], v[144:147], v[84:99]
	s_waitcnt lgkmcnt(0)
	v_mfma_f32_32x32x16_bf16 v[68:83], v[228:231], v[144:147], v[68:83]
	s_setprio 0
	s_nop 8
	v_max_f32_e32 v66, v85, v85
	v_max_f32_e32 v219, v84, v84
	v_max_f32_e32 v66, v219, v66
	v_max3_f32 v66, v66, v86, v87
	v_max3_f32 v66, v66, v88, v89
	v_max3_f32 v66, v66, v90, v91
	v_max3_f32 v66, v66, v92, v93
	v_max3_f32 v66, v66, v94, v95
	v_max3_f32 v66, v66, v96, v97
	v_max3_f32 v66, v66, v98, v99
	v_max3_f32 v66, v66, v68, v69
	v_max3_f32 v66, v66, v70, v71
	v_max3_f32 v66, v66, v72, v73
	v_max3_f32 v66, v66, v74, v75
	v_max3_f32 v66, v66, v76, v77
	v_max3_f32 v66, v66, v78, v79
	v_max3_f32 v66, v66, v80, v81
	v_max3_f32 v66, v66, v82, v83
	v_mov_b32_e32 v219, v66
	s_nop 1
	v_permlane32_swap_b32_e32 v66, v219
	v_max_f32_e32 v219, v219, v219
	v_max_f32_e32 v66, v66, v66
	v_max_f32_e32 v66, v66, v219
	v_max_f32_e32 v220, v215, v215
	v_sub_f32_e32 v219, v66, v215
	v_max_f32_e32 v66, v220, v66
	v_sub_f32_e32 v220, v215, v66
	v_mul_f32_e32 v220, 0x3dd53b94, v220
	v_exp_f32_e32 v220, v220
	v_cmp_ge_f32_e32 vcc, s31, v219
	s_cmp_eq_u64 vcc, exec
	s_cselect_b64 s[6:7], -1, 0
	v_cndmask_b32_e64 v219, v220, 1.0, s[6:7]
	v_cmp_gt_f32_e32 vcc, 1.0, v219
	s_cbranch_vccz .LBB0_911
; DEV void partialSM(f32x16& p0, f32x16& p1, float& m_reg, float& mn, float& alpha) {
;     ...
;   const float mnC = -mn * C;
; #pragma unroll
;   for (int r = 0; r < 16; ++r) p0[r] = fmaf(p0[r], C, mnC);
; #pragma unroll
;   for (int r = 0; r < 16; ++r) p1[r] = fmaf(p1[r], C, mnC);
; #pragma unroll
;   for (int r = 0; r < 16; ++r) p0[r] = __builtin_amdgcn_exp2f(p0[r]);
; }
; DEV void finishSM(f32x16& p0, f32x16& p1, float alpha, float& l_reg, bf16x8& pa0, bf16x8& pa1, bf16x8& pa2, bf16x8& pa3) {
; #pragma unroll
;   for (int r = 0; r < 16; ++r) p1[r] = __builtin_amdgcn_exp2f(p1[r]);
;   float ps = 0;
; #pragma unroll
;   for (int r = 0; r < 16; ++r) ps += p0[r];
; #pragma unroll
;   for (int r = 0; r < 16; ++r) ps += p1[r];
;   { auto rr = __builtin_amdgcn_permlane32_swap(__float_as_uint(ps), __float_as_uint(ps), false, false);
;     ps = __uint_as_float(rr[0]) + __uint_as_float(rr[1]); }
;   l_reg = l_reg * alpha + ps;
;     ...
;   PK4(p0, 0, pa0); PK4(p0, 8, pa1); PK4(p1, 0, pa2); PK4(p1, 8, pa3);
;     ...
; }
; DEV void qkt(f32x16& p0, f32x16& p1, const char* Ks, const bf16x8* qr, int r32, int hi) {
;   p0 = f32x16{}; p1 = f32x16{};
;   __builtin_amdgcn_s_setprio(1);
; #pragma unroll
;   for (int d0 = 0; d0 < 12; ++d0) { const int cb = (d0 * 16 + hi * 8) * 2;
;     const bf16x8 b0 = *reinterpret_cast<const bf16x8*>(Ks + KSWZ2(r32, cb));
;     const bf16x8 b1 = *reinterpret_cast<const bf16x8*>(Ks + KSWZ2(32 + r32, cb));
;     p0 = __builtin_amdgcn_mfma_f32_32x32x16_bf16(b0, qr[d0], p0, 0, 0, 0);
;     p1 = __builtin_amdgcn_mfma_f32_32x32x16_bf16(b1, qr[d0], p1, 0, 0, 0); }
;   __builtin_amdgcn_s_setprio(0);
; }
; DEV int v_st(int k, int c) { const int kk = (k & ~0xC) | ((k & 4) << 1) | ((k & 8) >> 1); return ((kk >> 3) * 4 + (c >> 5)) * 512 + ((kk & 7) * 32 + (c & 31)) * 2; }
; DEV int v_rd_base(int lane) { return ((lane & 3) << 3) | (((lane >> 2) & 3) << 6) | (((lane >> 4) & 1) << 5) | (((lane >> 5) & 1) << 8); }
; template <int OFF> DEV s16x4 tr_read(int vb) { s16x4 r; asm volatile("ds_read_b64_tr_b16 %0, %1 offset:%2" : "=&v"(r) : "v"(vb), "i"(OFF) : "memory"); return r; }
; template <int D0> DEV void pv_read(VFrag& f, int vb) {
;   f.l0 = tr_read<v_rd_off(D0, 0, 0)>(vb); f.h0 = tr_read<v_rd_off(D0, 0, 1)>(vb); f.l1 = tr_read<v_rd_off(D0, 1, 0)>(vb); f.h1 = tr_read<v_rd_off(D0, 1, 1)>(vb);
	s_and_saveexec_b64 s[24:25], s[4:5]
	ds_write_b32 v210, v219 offset:128
	s_or_b64 exec, exec, s[24:25]
	s_waitcnt lgkmcnt(0)
	v_add_u32_e32 v220, v185, v186
	ds_read_b128 v[224:227], v220 offset:224
	ds_read_b128 v[228:231], v220 offset:192
	ds_read_b128 v[232:235], v220 offset:160
	ds_read_b128 v[236:239], v220 offset:128
	s_waitcnt lgkmcnt(3)
	v_pk_mul_f32 v[62:63], v[62:63], v[224:225]
	s_waitcnt lgkmcnt(2)
	v_pk_mul_f32 v[58:59], v[58:59], v[228:229]
	s_waitcnt lgkmcnt(1)
	v_pk_mul_f32 v[54:55], v[54:55], v[232:233]
	v_pk_mul_f32 v[64:65], v[64:65], v[226:227]
	v_pk_mul_f32 v[60:61], v[60:61], v[230:231]
	v_pk_mul_f32 v[56:57], v[56:57], v[234:235]
	s_waitcnt lgkmcnt(0)
	v_pk_mul_f32 v[52:53], v[52:53], v[238:239]
	v_pk_mul_f32 v[50:51], v[50:51], v[236:237]
	v_pk_mul_f32 v[46:47], v[46:47], v[224:225]
	v_pk_mul_f32 v[42:43], v[42:43], v[228:229]
	v_pk_mul_f32 v[38:39], v[38:39], v[232:233]
	v_pk_mul_f32 v[48:49], v[48:49], v[226:227]
	v_pk_mul_f32 v[44:45], v[44:45], v[230:231]
	v_pk_mul_f32 v[40:41], v[40:41], v[234:235]
	v_pk_mul_f32 v[36:37], v[36:37], v[238:239]
	v_pk_mul_f32 v[34:35], v[34:35], v[236:237]
	v_pk_mul_f32 v[30:31], v[30:31], v[224:225]
	v_pk_mul_f32 v[26:27], v[26:27], v[228:229]
	v_pk_mul_f32 v[22:23], v[22:23], v[232:233]
	v_pk_mul_f32 v[32:33], v[32:33], v[226:227]
	v_pk_mul_f32 v[28:29], v[28:29], v[230:231]
	v_pk_mul_f32 v[24:25], v[24:25], v[234:235]
	v_pk_mul_f32 v[20:21], v[20:21], v[238:239]
	v_pk_mul_f32 v[18:19], v[18:19], v[236:237]
	v_pk_mul_f32 v[14:15], v[14:15], v[224:225]
	v_pk_mul_f32 v[10:11], v[10:11], v[228:229]
	v_pk_mul_f32 v[6:7], v[6:7], v[232:233]
	v_pk_mul_f32 v[16:17], v[16:17], v[226:227]
	v_pk_mul_f32 v[12:13], v[12:13], v[230:231]
	v_pk_mul_f32 v[8:9], v[8:9], v[234:235]
	v_pk_mul_f32 v[4:5], v[4:5], v[238:239]
	v_pk_mul_f32 v[2:3], v[2:3], v[236:237]
.LBB0_911:
	v_cndmask_b32_e64 v215, v66, v215, s[6:7]
	v_mul_f32_e32 v66, 0xbdd53b94, v215
	v_fmamk_f32 v84, v84, 0x3dd53b94, v66
	v_fmamk_f32 v85, v85, 0x3dd53b94, v66
	v_fmamk_f32 v86, v86, 0x3dd53b94, v66
	v_fmamk_f32 v87, v87, 0x3dd53b94, v66
	v_fmamk_f32 v88, v88, 0x3dd53b94, v66
	v_fmamk_f32 v89, v89, 0x3dd53b94, v66
	v_fmamk_f32 v90, v90, 0x3dd53b94, v66
	v_fmamk_f32 v91, v91, 0x3dd53b94, v66
	v_fmamk_f32 v92, v92, 0x3dd53b94, v66
	v_fmamk_f32 v93, v93, 0x3dd53b94, v66
	v_fmamk_f32 v94, v94, 0x3dd53b94, v66
	v_fmamk_f32 v95, v95, 0x3dd53b94, v66
	v_fmamk_f32 v96, v96, 0x3dd53b94, v66
	v_fmamk_f32 v97, v97, 0x3dd53b94, v66
	v_fmamk_f32 v98, v98, 0x3dd53b94, v66
	v_fmamk_f32 v99, v99, 0x3dd53b94, v66
	v_fmamk_f32 v68, v68, 0x3dd53b94, v66
	v_fmamk_f32 v69, v69, 0x3dd53b94, v66
	v_fmamk_f32 v70, v70, 0x3dd53b94, v66
	v_fmamk_f32 v71, v71, 0x3dd53b94, v66
	v_fmamk_f32 v72, v72, 0x3dd53b94, v66
	v_fmamk_f32 v73, v73, 0x3dd53b94, v66
	v_fmamk_f32 v74, v74, 0x3dd53b94, v66
	v_fmamk_f32 v75, v75, 0x3dd53b94, v66
	v_fmamk_f32 v76, v76, 0x3dd53b94, v66
	v_fmamk_f32 v77, v77, 0x3dd53b94, v66
	v_fmamk_f32 v78, v78, 0x3dd53b94, v66
	v_fmamk_f32 v79, v79, 0x3dd53b94, v66
	v_fmamk_f32 v80, v80, 0x3dd53b94, v66
	v_fmamk_f32 v81, v81, 0x3dd53b94, v66
	v_fmamk_f32 v82, v82, 0x3dd53b94, v66
	v_fmac_f32_e32 v66, 0x3dd53b94, v83
	v_exp_f32_e32 v83, v84
	v_exp_f32_e32 v84, v85
	v_exp_f32_e32 v85, v86
	v_exp_f32_e32 v86, v87
	v_exp_f32_e32 v87, v88
	v_exp_f32_e32 v88, v89
	v_exp_f32_e32 v89, v90
	v_exp_f32_e32 v90, v91
	v_exp_f32_e32 v91, v92
	v_exp_f32_e32 v92, v93
	v_exp_f32_e32 v93, v94
	v_exp_f32_e32 v94, v95
	v_exp_f32_e32 v95, v96
	v_exp_f32_e32 v96, v97
	v_exp_f32_e32 v97, v98
	v_exp_f32_e32 v98, v99
	v_exp_f32_e32 v99, v68
	v_add_f32_e32 v68, 0, v83
	v_add_f32_e32 v68, v84, v68
	v_add_f32_e32 v68, v85, v68
	v_add_f32_e32 v68, v86, v68
	v_add_f32_e32 v68, v87, v68
	v_add_f32_e32 v68, v88, v68
	v_add_f32_e32 v68, v89, v68
	v_add_f32_e32 v68, v90, v68
	v_add_f32_e32 v68, v91, v68
	v_add_f32_e32 v68, v92, v68
	v_add_f32_e32 v68, v93, v68
	v_add_f32_e32 v68, v94, v68
	v_add_f32_e32 v68, v95, v68
	v_exp_f32_e32 v220, v69
	v_add_f32_e32 v68, v96, v68
	v_exp_f32_e32 v221, v70
	v_add_f32_e32 v68, v97, v68
	v_exp_f32_e32 v222, v71
	v_add_f32_e32 v68, v98, v68
	v_exp_f32_e32 v224, v72
	v_add_f32_e32 v68, v99, v68
	v_exp_f32_e32 v225, v73
	v_add_f32_e32 v68, v220, v68
	v_exp_f32_e32 v226, v74
	v_add_f32_e32 v68, v221, v68
	v_exp_f32_e32 v227, v75
	v_add_f32_e32 v68, v222, v68
	v_exp_f32_e32 v228, v76
	v_add_f32_e32 v68, v224, v68
	v_exp_f32_e32 v229, v77
	v_add_f32_e32 v68, v225, v68
	v_exp_f32_e32 v230, v78
	v_add_f32_e32 v68, v226, v68
	v_exp_f32_e32 v231, v79
	v_add_f32_e32 v68, v227, v68
	v_exp_f32_e32 v232, v80
	v_add_f32_e32 v68, v228, v68
	v_exp_f32_e32 v233, v81
	v_add_f32_e32 v68, v229, v68
	v_exp_f32_e32 v234, v82
	v_add_f32_e32 v68, v230, v68
	v_exp_f32_e32 v66, v66
	v_add_f32_e32 v68, v231, v68
	v_add_f32_e32 v68, v232, v68
	v_add_f32_e32 v68, v233, v68
	v_add_f32_e32 v68, v234, v68
	v_add_f32_e32 v68, v66, v68
	v_mov_b32_e32 v69, v68
	s_nop 1
	v_permlane32_swap_b32_e32 v68, v69
	v_cvt_pk_bf16_f32 v70, v83, v84
	v_cvt_pk_bf16_f32 v71, v85, v86
	v_cvt_pk_bf16_f32 v72, v87, v88
	v_cvt_pk_bf16_f32 v73, v89, v90
	v_cvt_pk_bf16_f32 v74, v91, v92
	v_cvt_pk_bf16_f32 v75, v93, v94
	v_cvt_pk_bf16_f32 v76, v95, v96
	v_cvt_pk_bf16_f32 v77, v97, v98
	v_cvt_pk_bf16_f32 v78, v99, v220
	v_cvt_pk_bf16_f32 v79, v221, v222
	v_cvt_pk_bf16_f32 v80, v224, v225
	v_cvt_pk_bf16_f32 v81, v226, v227
	v_cvt_pk_bf16_f32 v82, v228, v229
	v_cvt_pk_bf16_f32 v83, v230, v231
	v_cvt_pk_bf16_f32 v84, v232, v233
	v_cvt_pk_bf16_f32 v85, v234, v66
	v_permlane32_swap_b32_e32 v70, v72
	v_permlane32_swap_b32_e32 v71, v73
	v_permlane32_swap_b32_e32 v74, v76
	v_permlane32_swap_b32_e32 v75, v77
	v_permlane32_swap_b32_e32 v78, v80
	v_permlane32_swap_b32_e32 v79, v81
	v_permlane32_swap_b32_e32 v82, v84
	v_permlane32_swap_b32_e32 v83, v85
	v_lshl_add_u32 v66, s36, 14, v214
	ds_read_b64_tr_b16 v[86:87], v66 offset:0
	ds_read_b64_tr_b16 v[88:89], v66 offset:0x800
	ds_read_b64_tr_b16 v[90:91], v66 offset:0x1000
	ds_read_b64_tr_b16 v[92:93], v66 offset:0x1800
	ds_read_b64_tr_b16 v[94:95], v66 offset:0x2000
	ds_read_b64_tr_b16 v[96:97], v66 offset:0x2800
	ds_read_b64_tr_b16 v[224:225], v66 offset:0x3000
	ds_read_b64_tr_b16 v[226:227], v66 offset:0x3800
	ds_read_b64_tr_b16 v[228:229], v66 offset:0x200
	ds_read_b64_tr_b16 v[230:231], v66 offset:0xa00
	ds_read_b64_tr_b16 v[232:233], v66 offset:0x1200
	ds_read_b64_tr_b16 v[234:235], v66 offset:0x1a00
	ds_read_b64_tr_b16 v[236:237], v66 offset:0x2200
	ds_read_b64_tr_b16 v[238:239], v66 offset:0x2a00
	ds_read_b64_tr_b16 v[240:241], v66 offset:0x3200
	ds_read_b64_tr_b16 v[242:243], v66 offset:0x3a00
	s_waitcnt lgkmcnt(8)
; DEV int ltid() { int t = threadIdx.x; asm volatile("" : "+v"(t)); return t; }
; DEV unsigned cvt_pk4_fp8(f32x4 v) { unsigned r = 0; r = __builtin_amdgcn_cvt_pk_fp8_f32(v[0], v[1], r, false); r = __builtin_amdgcn_cvt_pk_fp8_f32(v[2], v[3], r, true); return r; }
; #define SBAR() __builtin_amdgcn_sched_barrier(0)
; #define PV_WAIT(n) do { asm volatile("s_waitcnt lgkmcnt(" #n ")" ::: "memory"); SBAR(); } while (0)
; DEV void fill_load(CParams& p, int wg, int slot, f32x4 (&ld)[4]) {
;   const FillDesc d = fill_decode(p, wg, slot); const int tid = ltid(), tx = tid & 15, ty = tid >> 4;
;   const float* sp = d.src + (long)(d.kh + 4 * ty) * d.ldsrc + d.n0 + 4 * tx;
; #pragma unroll
;   for (int r = 0; r < 4; ++r) ld[r] = *(const f32x4*)(sp + (long)r * d.ldsrc);
; }
; DEV void fill_write(const f32x4 (&ld)[4], int bufsel) {
;   extern __shared__ __attribute__((aligned(16))) char shm[];
;   unsigned* T = (unsigned*)(shm + FILL_LDS_OFF + bufsel * FILL_TB); const int tid = ltid(), tx = tid & 15, ty = tid >> 4;
;   constexpr float WS = (float)(1 << FP8_WSCALE_LOG2_);
; #pragma unroll
;   for (int j = 0; j < 4; ++j) T[(4 * tx + j) * 33 + ty] = cvt_pk4_fp8((f32x4){ld[0][j] * WS, ld[1][j] * WS, ld[2][j] * WS, ld[3][j] * WS});
; }
; DEV void pv_d0(f32x16* o, int vb, bf16x8 pa0, bf16x8 pa1, bf16x8 pa2, bf16x8 pa3) {
;   VFrag fa, fb;
;   pv_read<0>(fa, vb);
;   pv_read<1>(fb, vb); PV_WAIT(8); pv_mma(o[0], fa, pa0, pa1, pa2, pa3); SBAR();
;   pv_read<2>(fa, vb); PV_WAIT(8); pv_mma(o[1], fb, pa0, pa1, pa2, pa3); SBAR();
;   pv_read<3>(fb, vb); PV_WAIT(8); pv_mma(o[2], fa, pa0, pa1, pa2, pa3); SBAR();
;   PV_WAIT(0); pv_mma(o[3], fb, pa0, pa1, pa2, pa3);
	s_setprio 1
	v_mfma_f32_32x32x16_bf16 v[50:65], v[70:73], v[86:89], v[50:65]
	v_mfma_f32_32x32x16_bf16 v[50:65], v[74:77], v[90:93], v[50:65]
	v_mfma_f32_32x32x16_bf16 v[50:65], v[78:81], v[94:97], v[50:65]
	v_mfma_f32_32x32x16_bf16 v[50:65], v[82:85], v[224:227], v[50:65]
	s_setprio 0
	ds_read_b64_tr_b16 v[86:87], v66 offset:0x400
	ds_read_b64_tr_b16 v[88:89], v66 offset:0xc00
	ds_read_b64_tr_b16 v[90:91], v66 offset:0x1400
	ds_read_b64_tr_b16 v[92:93], v66 offset:0x1c00
	ds_read_b64_tr_b16 v[94:95], v66 offset:0x2400
	ds_read_b64_tr_b16 v[96:97], v66 offset:0x2c00
	ds_read_b64_tr_b16 v[224:225], v66 offset:0x3400
	ds_read_b64_tr_b16 v[226:227], v66 offset:0x3c00
	s_waitcnt lgkmcnt(8)
	s_setprio 1
	v_mfma_f32_32x32x16_bf16 v[34:49], v[70:73], v[228:231], v[34:49]
	v_mfma_f32_32x32x16_bf16 v[34:49], v[74:77], v[232:235], v[34:49]
	v_mfma_f32_32x32x16_bf16 v[34:49], v[78:81], v[236:239], v[34:49]
	v_mfma_f32_32x32x16_bf16 v[34:49], v[82:85], v[240:243], v[34:49]
	s_setprio 0
	ds_read_b64_tr_b16 v[228:229], v66 offset:0x600
	ds_read_b64_tr_b16 v[230:231], v66 offset:0xe00
	ds_read_b64_tr_b16 v[232:233], v66 offset:0x1600
	ds_read_b64_tr_b16 v[234:235], v66 offset:0x1e00
	ds_read_b64_tr_b16 v[236:237], v66 offset:0x2600
	ds_read_b64_tr_b16 v[238:239], v66 offset:0x2e00
	ds_read_b64_tr_b16 v[240:241], v66 offset:0x3600
	ds_read_b64_tr_b16 v[242:243], v66 offset:0x3e00
	s_waitcnt lgkmcnt(8)
	s_setprio 1
	v_mfma_f32_32x32x16_bf16 v[18:33], v[70:73], v[86:89], v[18:33]
	v_mfma_f32_32x32x16_bf16 v[18:33], v[74:77], v[90:93], v[18:33]
	v_mfma_f32_32x32x16_bf16 v[18:33], v[78:81], v[94:97], v[18:33]
	v_mfma_f32_32x32x16_bf16 v[18:33], v[82:85], v[224:227], v[18:33]
	s_setprio 0
	s_waitcnt lgkmcnt(0)
	s_setprio 1
	v_mfma_f32_32x32x16_bf16 v[2:17], v[70:73], v[228:231], v[2:17]
	v_mfma_f32_32x32x16_bf16 v[2:17], v[74:77], v[232:235], v[2:17]
	v_mfma_f32_32x32x16_bf16 v[2:17], v[78:81], v[236:239], v[2:17]
	v_mfma_f32_32x32x16_bf16 v[2:17], v[82:85], v[240:243], v[2:17]
	s_setprio 0
	s_cmp_gt_u32 s37, 62
	s_cbranch_scc1 .LBB0_919
	s_waitcnt vmcnt(3)
	v_mul_f32_e32 v71, 0x42800000, v168
	s_waitcnt vmcnt(2)
	v_mul_f32_e32 v72, 0x42800000, v172
	v_cvt_pk_fp8_f32 v73, v71, v72
	s_waitcnt vmcnt(1)
	v_mul_f32_e32 v71, 0x42800000, v176
	s_waitcnt vmcnt(0)
	v_mul_f32_e32 v72, 0x42800000, v180
	v_cvt_pk_fp8_f32 v73, v71, v72 op_sel:[0,0,1]
	v_mul_f32_e32 v71, 0x42800000, v169
	v_mul_f32_e32 v72, 0x42800000, v173
	v_cvt_pk_fp8_f32 v74, v71, v72
	v_mul_f32_e32 v71, 0x42800000, v177
	v_mul_f32_e32 v72, 0x42800000, v181
	v_cvt_pk_fp8_f32 v74, v71, v72 op_sel:[0,0,1]
	v_mul_f32_e32 v71, 0x42800000, v170
	v_mul_f32_e32 v72, 0x42800000, v174
	v_cvt_pk_fp8_f32 v77, v71, v72
	v_mul_f32_e32 v71, 0x42800000, v171
	v_mul_f32_e32 v72, 0x42800000, v175
	v_cvt_pk_fp8_f32 v78, v71, v72
	v_mul_f32_e32 v75, 0x42800000, v178
	v_mul_f32_e32 v76, 0x42800000, v182
	v_mul_f32_e32 v71, 0x42800000, v179
	v_mul_f32_e32 v72, 0x42800000, v183
	v_cvt_pk_fp8_f32 v77, v75, v76 op_sel:[0,0,1]
	v_cvt_pk_fp8_f32 v78, v71, v72 op_sel:[0,0,1]
	s_mul_i32 s56, s36, 0x2200
	s_cmp_eq_u32 s34, 60
	v_add_u32_e32 v66, s56, v245
	ds_write2_b32 v66, v73, v74 offset1:33
	ds_write2_b32 v66, v77, v78 offset0:66 offset1:99
	s_cbranch_scc1 .LBB0_919
	s_cmp_lg_u32 s37, 60
	s_cbranch_scc1 .Lfld_a
	s_mov_b64 s[62:63], s[20:21]
	v_mov_b32_e32 v248, v252
	v_add_u32_e32 v249, 0x2000, v252
	v_add_u32_e32 v250, 0x4000, v252
	v_add_u32_e32 v251, 0x6000, v252
.Lfld_a:
	global_load_dwordx4 v[168:171], v248, s[62:63]
	global_load_dwordx4 v[172:175], v249, s[62:63]
	global_load_dwordx4 v[176:179], v250, s[62:63]
	global_load_dwordx4 v[180:183], v251, s[62:63]
	s_add_u32 s62, s62, 0x800000
	s_addc_u32 s63, s63, 0

; DEV int ltid() { int t = threadIdx.x; asm volatile("" : "+v"(t)); return t; }
; DEV unsigned cvt_pk_bf16(float lo, float hi) { const f32x2 v = {lo, hi}; const bf16n2 r = __builtin_convertvector(v, bf16n2); return __builtin_bit_cast(unsigned, r); }
; DEV float bf2f(bf16_t v) { return __uint_as_float(((unsigned)v) << 16); }
; DEV int v_st(int k, int c) { const int kk = (k & ~0xC) | ((k & 4) << 1) | ((k & 8) >> 1); return ((kk >> 3) * 4 + (c >> 5)) * 512 + ((kk & 7) * 32 + (c & 31)) * 2; }
; DEV void fill_load(CParams& p, int wg, int slot, f32x4 (&ld)[4]) {
;   const FillDesc d = fill_decode(p, wg, slot); const int tid = ltid(), tx = tid & 15, ty = tid >> 4;
;   const float* sp = d.src + (long)(d.kh + 4 * ty) * d.ldsrc + d.n0 + 4 * tx;
; #pragma unroll
;   for (int r = 0; r < 4; ++r) ld[r] = *(const f32x4*)(sp + (long)r * d.ldsrc);
; DEV void attn_unit(const bf16_t* __restrict__ Qb, const bf16_t* __restrict__ Kh, const bf16_t* __restrict__ Vh, const float* __restrict__ rp, bf16_t* __restrict__ Ob, CParams& fp, int fwg, int fbase, int fn) {
;     ...
; #pragma unroll
;     for (int dd = 0; dd < 2; ++dd) {
;       const int a0 = 16 * dd + 8 * hi;
;       const f32x4 c0 = *(const f32x4*)(rr + a0), c1 = *(const f32x4*)(rr + a0 + 4), s0 = *(const f32x4*)(rr + 32 + a0), s1 = *(const f32x4*)(rr + 32 + a0 + 4);
;       float cs[8] = {c0[0], c0[1], c0[2], c0[3], c1[0], c1[1], c1[2], c1[3]}, sn[8] = {s0[0], s0[1], s0[2], s0[3], s1[0], s1[1], s1[2], s1[3]};
;       const bf16x8 x1 = qr[8 + dd], x2 = qr[10 + dd]; bf16x8 y1, y2;
; #pragma unroll
;       for (int j = 0; j < 8; j += 2) {
;         const float a1 = bf2f((bf16_t)x1[j]), a2 = bf2f((bf16_t)x2[j]), b1 = bf2f((bf16_t)x1[j + 1]), b2 = bf2f((bf16_t)x2[j + 1]);
;         const unsigned u1 = cvt_pk_bf16(a1 * cs[j] - a2 * sn[j], b1 * cs[j + 1] - b2 * sn[j + 1]);
;         const unsigned u2 = cvt_pk_bf16(a1 * sn[j] + a2 * cs[j], b1 * sn[j + 1] + b2 * cs[j + 1]);
;         y1[j] = (short)(u1 & 0xffff); y1[j + 1] = (short)(u1 >> 16); y2[j] = (short)(u2 & 0xffff); y2[j + 1] = (short)(u2 >> 16);
;       }
;       qr[8 + dd] = y1; qr[10 + dd] = y2;
;     }
;   }
;   const int sr = tid >> 4, sc = (tid & 15) * 8, vst0 = v_st(sr, sc), vst1 = v_st(32 + sr, sc);
;   int kst[3];
; #pragma unroll
;   for (int i = 0; i < 3; ++i) { const int id = tid + 512 * i, row = id / 24, ch = id % 24; kst[i] = KSWZ2(row, ch * 16); }
.LBB0_1097:
	s_waitcnt vmcnt(11)
	v_and_b32_e32 v81, 0xffff0000, v58
	v_lshlrev_b32_e32 v80, 16, v58
	s_waitcnt vmcnt(9)
	v_and_b32_e32 v83, 0xffff0000, v50
	v_lshlrev_b32_e32 v82, 16, v50
	s_waitcnt vmcnt(4)
	v_pk_mul_f32 v[84:85], v[66:67], v[82:83]
	v_pk_mul_f32 v[66:67], v[66:67], v[80:81]
	v_pk_fma_f32 v[84:85], v[62:63], v[80:81], v[84:85] neg_lo:[0,0,1] neg_hi:[0,0,1]
	v_pk_fma_f32 v[62:63], v[62:63], v[82:83], v[66:67]
	v_lshlrev_b32_e32 v58, 16, v51
	v_cvt_pk_bf16_f32 v136, v62, v63
	v_and_b32_e32 v63, 0xffff0000, v59
	v_lshlrev_b32_e32 v62, 16, v59
	v_and_b32_e32 v59, 0xffff0000, v51
	v_pk_mul_f32 v[50:51], v[68:69], v[58:59]
	s_mov_b32 s21, 0x2aaaaaab
	v_pk_fma_f32 v[50:51], v[64:65], v[62:63], v[50:51] neg_lo:[0,0,1] neg_hi:[0,0,1]
	s_lshl_b32 s23, s17, 7
	v_cvt_pk_bf16_f32 v133, v50, v51
	v_pk_mul_f32 v[50:51], v[68:69], v[62:63]
	s_lshl_b32 s17, s17, s22
	v_pk_fma_f32 v[50:51], v[64:65], v[58:59], v[50:51]
	v_and_b32_e32 v59, 0xffff0000, v52
	v_lshlrev_b32_e32 v58, 16, v52
	v_cvt_pk_bf16_f32 v137, v50, v51
	v_and_b32_e32 v51, 0xffff0000, v60
	v_lshlrev_b32_e32 v50, 16, v60
	v_pk_mul_f32 v[62:63], v[54:55], v[58:59]
	s_and_b32 s17, s17, 0x780
	v_pk_fma_f32 v[62:63], v[46:47], v[50:51], v[62:63] neg_lo:[0,0,1] neg_hi:[0,0,1]
	v_pk_mul_f32 v[50:51], v[54:55], v[50:51]
	s_and_b32 s18, s18, s23
	v_pk_fma_f32 v[46:47], v[46:47], v[58:59], v[50:51]
	v_and_b32_e32 v51, 0xffff0000, v53
	v_lshlrev_b32_e32 v50, 16, v53
	v_cvt_pk_bf16_f32 v138, v46, v47
	v_and_b32_e32 v47, 0xffff0000, v61
	v_lshlrev_b32_e32 v46, 16, v61
	v_pk_mul_f32 v[52:53], v[56:57], v[50:51]
	s_or_b32 s18, s18, s53
	v_pk_fma_f32 v[52:53], v[48:49], v[46:47], v[52:53] neg_lo:[0,0,1] neg_hi:[0,0,1]
	v_pk_mul_f32 v[46:47], v[56:57], v[46:47]
	s_mov_b32 s19, 0
	v_pk_fma_f32 v[46:47], v[48:49], v[50:51], v[46:47]
	v_and_b32_e32 v49, 0xffff0000, v22
	v_cvt_pk_bf16_f32 v139, v46, v47
	v_and_b32_e32 v47, 0xffff0000, v30
	v_lshlrev_b32_e32 v46, 16, v30
	v_lshlrev_b32_e32 v48, 16, v22
	s_waitcnt vmcnt(0)
	v_pk_mul_f32 v[50:51], v[42:43], v[48:49]
	v_pk_mul_f32 v[42:43], v[42:43], v[46:47]
	v_pk_fma_f32 v[50:51], v[38:39], v[46:47], v[50:51] neg_lo:[0,0,1] neg_hi:[0,0,1]
	v_pk_fma_f32 v[38:39], v[38:39], v[48:49], v[42:43]
	v_lshlrev_b32_e32 v30, 16, v23
	v_cvt_pk_bf16_f32 v144, v38, v39
	v_and_b32_e32 v39, 0xffff0000, v31
	v_lshlrev_b32_e32 v38, 16, v31
	v_and_b32_e32 v31, 0xffff0000, v23
	v_pk_mul_f32 v[22:23], v[44:45], v[30:31]
	s_lshl_b32 s18, s18, 2
	v_pk_fma_f32 v[22:23], v[40:41], v[38:39], v[22:23] neg_lo:[0,0,1] neg_hi:[0,0,1]
	v_mov_b32_e32 v67, 0
	v_cvt_pk_bf16_f32 v141, v22, v23
	v_pk_mul_f32 v[22:23], v[44:45], v[38:39]
	v_mov_b32_e32 v253, v67
	v_pk_fma_f32 v[22:23], v[40:41], v[30:31], v[22:23]
	v_and_b32_e32 v31, 0xffff0000, v24
	v_lshlrev_b32_e32 v30, 16, v24
	v_cvt_pk_bf16_f32 v145, v22, v23
	v_and_b32_e32 v23, 0xffff0000, v32
	v_lshlrev_b32_e32 v22, 16, v32
	v_pk_mul_f32 v[38:39], v[34:35], v[30:31]
	v_and_b32_e32 v77, 0x3fffffc0, v1
	v_pk_fma_f32 v[38:39], v[26:27], v[22:23], v[38:39] neg_lo:[0,0,1] neg_hi:[0,0,1]
	v_pk_mul_f32 v[22:23], v[34:35], v[22:23]
	v_lshl_add_u32 v185, v77, 2, s77
	v_pk_fma_f32 v[22:23], v[26:27], v[30:31], v[22:23]
	v_and_b32_e32 v27, 0xffff0000, v25
	v_lshlrev_b32_e32 v26, 16, v25
	v_cvt_pk_bf16_f32 v146, v22, v23
	v_and_b32_e32 v23, 0xffff0000, v33
	v_lshlrev_b32_e32 v22, 16, v33
	v_pk_mul_f32 v[24:25], v[36:37], v[26:27]
	v_cvt_pk_bf16_f32 v134, v62, v63
	v_pk_fma_f32 v[24:25], v[28:29], v[22:23], v[24:25] neg_lo:[0,0,1] neg_hi:[0,0,1]
	v_pk_mul_f32 v[22:23], v[36:37], v[22:23]
	v_cvt_pk_bf16_f32 v143, v24, v25
	v_pk_fma_f32 v[22:23], v[28:29], v[26:27], v[22:23]
	v_and_b32_e32 v25, 3, v74
	v_cvt_pk_bf16_f32 v147, v22, v23
	v_and_b32_e32 v22, 0xfffff0, v74
	v_lshlrev_b32_e32 v23, 1, v74
	v_and_or_b32 v22, v23, 8, v22
	v_lshrrev_b32_e32 v23, 1, v74
	v_and_or_b32 v23, v23, 4, v25
	v_and_b32_e32 v25, 0xfffff0, v76
	v_lshlrev_b32_e32 v26, 1, v76
	v_and_or_b32 v25, v26, 8, v25
	v_lshrrev_b32_e32 v22, 1, v22
	v_lshrrev_b32_e32 v24, 5, v78
	v_lshrrev_b32_e32 v25, 1, v25
	v_or_b32_e32 v22, v22, v24
	v_or_b32_e32 v24, v25, v24
	v_mul_hi_i32 v25, v1, s21
	v_lshrrev_b32_e32 v26, 31, v25
	v_ashrrev_i32_e32 v25, 2, v25
	v_add_u32_e32 v25, v25, v26
	v_mul_lo_u32 v26, v25, 24
	v_sub_u32_e32 v26, v1, v26
	v_lshlrev_b32_e32 v27, 9, v25
	v_bitop3_b32 v25, v25, v26, 15 bitop3:0x6c
	v_lshl_add_u32 v195, v25, 4, v27
	v_add_u32_e32 v25, 0x200, v1
	v_mul_hi_i32 v26, v25, s21
	v_lshrrev_b32_e32 v27, 31, v26
	v_ashrrev_i32_e32 v26, 2, v26
	v_add_u32_e32 v26, v26, v27
	v_mul_lo_u32 v27, v26, 24
	v_sub_u32_e32 v25, v25, v27
	v_lshlrev_b32_e32 v27, 9, v26
	v_bitop3_b32 v25, v26, v25, 15 bitop3:0x6c
	v_lshl_add_u32 v196, v25, 4, v27
	v_add_u32_e32 v25, 0x400, v1
	v_mul_hi_i32 v26, v25, s21
	v_lshrrev_b32_e32 v27, 31, v26
	v_ashrrev_i32_e32 v26, 2, v26
	v_add_u32_e32 v26, v26, v27
	v_mul_lo_u32 v27, v26, 24
	v_sub_u32_e32 v25, v25, v27
	v_lshlrev_b32_e32 v27, 9, v26
	v_bitop3_b32 v25, v26, v25, 15 bitop3:0x6c
	v_lshlrev_b32_e32 v22, 9, v22
	v_lshlrev_b32_e32 v23, 6, v23
	v_lshl_add_u32 v197, v25, 4, v27
	v_and_b32_e32 v25, 48, v252
	v_lshlrev_b32_e32 v24, 9, v24
	v_or3_b32 v198, v22, v23, v25
	v_lshlrev_b32_e32 v22, 4, v187
	v_or3_b32 v199, v24, v23, v25
	v_and_b32_e32 v27, 0xc0, v22
	v_lshlrev_b32_e32 v22, 1, v187
	v_mov_b32_e32 v24, v0
	v_and_b32_e32 v28, 32, v22
	v_lshlrev_b32_e32 v26, 3, v187
	v_ashrrev_i32_e32 v22, 2, v24
	v_and_b32_e32 v22, -4, v22
	v_add_u32_e32 v22, s17, v22
	v_mad_i64_i32 v[22:23], s[22:23], s20, v22, 0
	v_lshl_add_u64 v[22:23], v[22:23], 2, s[14:15]
	v_lshlrev_b32_e32 v24, 4, v24
	v_lshl_add_u64 v[22:23], v[22:23], 0, s[18:19]
; DEV FillDesc fill_decode(CParams& p, int wg, int slot) {
;   const int h = slot * 256 + wg, t = h >> 1, half = h & 1; FillDesc d;
;   if (t < NE * 512) { const int e = t >> 9, r = t & 511; d.src = p.w_gu + (long)e * 2048 * 4096; d.ldsrc = 4096; d.dst = p.wt_gu8 + (long)e * 4096 * 2048; d.perm = 2; d.n0 = (r & 31) * 128 + 64 * half; d.kh = (r >> 5) * 128; }
;   else { const int v = t - NE * 512, e = v >> 8, r = v & 255; d.src = p.w_dn + (long)e * 2048 * 2048; d.ldsrc = 2048; d.dst = p.wt_dn8 + (long)e * 2048 * 2048; d.perm = 0; d.n0 = (r & 15) * 128 + 64 * half; d.kh = (r >> 4) * 128; }
;   return d;
; }
; DEV void fill_load(CParams& p, int wg, int slot, f32x4 (&ld)[4]) {
;   const FillDesc d = fill_decode(p, wg, slot); const int tid = ltid(), tx = tid & 15, ty = tid >> 4;
;   const float* sp = d.src + (long)(d.kh + 4 * ty) * d.ldsrc + d.n0 + 4 * tx;
; #pragma unroll
;   for (int r = 0; r < 4; ++r) ld[r] = *(const f32x4*)(sp + (long)r * d.ldsrc);
; }
; DEV void fill_write(const f32x4 (&ld)[4], int bufsel) {
;   extern __shared__ __attribute__((aligned(16))) char shm[];
;   unsigned* T = (unsigned*)(shm + FILL_LDS_OFF + bufsel * FILL_TB); const int tid = ltid(), tx = tid & 15, ty = tid >> 4;
;   constexpr float WS = (float)(1 << FP8_WSCALE_LOG2_);
; #pragma unroll
;   for (int j = 0; j < 4; ++j) T[(4 * tx + j) * 33 + ty] = cvt_pk4_fp8((f32x4){ld[0][j] * WS, ld[1][j] * WS, ld[2][j] * WS, ld[3][j] * WS});
; }
; DEV void fill_store(CParams& p, int wg, int slot, int bufsel) {
;   extern __shared__ __attribute__((aligned(16))) char shm[];
;   const unsigned* T = (const unsigned*)(shm + FILL_LDS_OFF + bufsel * FILL_TB); const int tid = ltid(), nl = tid >> 3, cc = tid & 7;
;   const FillDesc d = fill_decode(p, wg, slot);
;   u32x4 v; v.x = T[nl * 33 + 4 * cc]; v.y = T[nl * 33 + 4 * cc + 1]; v.z = T[nl * 33 + 4 * cc + 2]; v.w = T[nl * 33 + 4 * cc + 3];
;   *(u32x4*)(d.dst + (long)perm_row(d.perm, d.n0 + nl) * 2048 + d.kh + 16 * cc) = v;
; DEV void attn_unit(const bf16_t* __restrict__ Qb, const bf16_t* __restrict__ Kh, const bf16_t* __restrict__ Vh, const float* __restrict__ rp, bf16_t* __restrict__ Ob, CParams& fp, int fwg, int fbase, int fn) {
;     ...
;   f32x16 p0, p1; float mn, al; bf16x8 pa0, pa1, pa2, pa3; constexpr int NTL = KEYS / KVBLK;
;   f32x4 fld[4];
;   if (fn > 0) fill_load(fp, fwg, fbase, fld);
;   SWRITE(0); SLOAD(KVBLK); __syncthreads();
	v_and_b32_e32 v66, 0xf0, v24
	v_lshl_add_u64 v[22:23], v[22:23], 0, v[66:67]
	s_lshl_b32 s18, s20, 2
	v_lshl_add_u64 v[24:25], v[22:23], 0, s[18:19]
	global_load_dwordx4 v[168:171], v[22:23], off
	global_load_dwordx4 v[172:175], v[24:25], off
	v_lshl_add_u64 v[22:23], v[24:25], 0, s[18:19]
	v_lshl_add_u64 v[24:25], v[22:23], 0, s[18:19]
	global_load_dwordx4 v[176:179], v[22:23], off
	global_load_dwordx4 v[180:183], v[24:25], off
	v_add_u32_e32 v22, 0, v198
	ds_write_b128 v22, v[6:9]
	v_add_u32_e32 v6, 0, v199
	ds_write_b128 v6, v[2:5]
	v_add_u32_e32 v2, 0, v195
	ds_write_b128 v2, v[10:13] offset:32768
	v_add_u32_e32 v2, 0, v196
	ds_write_b128 v2, v[14:17] offset:32768
	v_add_u32_e32 v2, 0, v197
	ds_write_b128 v2, v[18:21] offset:32768
	v_lshlrev_b64 v[2:3], 8, v[74:75]
	v_lshl_add_u64 v[2:3], s[12:13], 0, v[2:3]
	v_lshl_add_u64 v[2:3], v[2:3], 0, v[252:253]
	s_movk_i32 s12, 0x4000
	v_add_co_u32_e32 v4, vcc, s12, v2
	s_movk_i32 s12, 0x6000
	s_nop 0
	v_addc_co_u32_e32 v5, vcc, 0, v3, vcc
	v_add_co_u32_e32 v2, vcc, s12, v2
	s_movk_i32 s17, 0xf0
	s_nop 0
	v_addc_co_u32_e32 v3, vcc, 0, v3, vcc
	global_load_dwordx4 v[148:151], v[4:5], off
	global_load_dwordx4 v[152:155], v[2:3], off
	v_lshlrev_b64 v[2:3], 1, v[72:73]
	v_lshl_add_u64 v[4:5], s[4:5], 0, v[2:3]
	v_add_co_u32_e32 v6, vcc, s12, v4
	s_mov_b32 s4, 0x8000
	s_nop 0
	v_addc_co_u32_e32 v7, vcc, 0, v5, vcc
	v_add_co_u32_e32 v8, vcc, s4, v4
	s_mov_b32 s4, 0xa000
	s_nop 0
	v_addc_co_u32_e32 v9, vcc, 0, v5, vcc
	v_add_co_u32_e32 v4, vcc, s4, v4
	global_load_dwordx4 v[156:159], v[6:7], off
	global_load_dwordx4 v[160:163], v[8:9], off
	v_addc_co_u32_e32 v5, vcc, 0, v5, vcc
	global_load_dwordx4 v[164:167], v[4:5], off
	v_lshlrev_b32_e32 v4, 4, v192
	v_and_b32_e32 v5, 0xf0, v4
	s_movk_i32 s4, 0x60
	v_bitop3_b32 v204, v186, v5, s4 bitop3:0x36
	s_movk_i32 s4, 0x80
	v_bitop3_b32 v205, v186, v5, s4 bitop3:0x36
	s_movk_i32 s4, 0xa0
	v_bitop3_b32 v206, v186, v5, s4 bitop3:0x36
	s_movk_i32 s4, 0xe0
	v_bitop3_b32 v208, v186, v5, s4 bitop3:0x36
	s_movk_i32 s4, 0x100
	v_bitop3_b32 v201, v186, v4, s17 bitop3:0x78
	v_bitop3_b32 v209, v186, v5, s4 bitop3:0x36
	s_movk_i32 s4, 0x120
	s_movk_i32 s17, 0x118
	s_cmp_lg_u32 0, -1
	v_bitop3_b32 v211, v186, v5, s4 bitop3:0x36
	s_movk_i32 s4, 0x140
	v_and_or_b32 v4, v26, s17, v28
	s_cselect_b32 s17, 0, 0
	s_movk_i32 s21, 0xc0
	v_bitop3_b32 v212, v186, v5, s4 bitop3:0x36
	s_movk_i32 s4, 0x160
	v_add3_u32 v214, v27, s17, v4
	s_add_i32 s17, s2, 0x8300
	v_mov_b32_e32 v4, 0x110000
	v_and_b32_e32 v6, 15, v1
	s_waitcnt lgkmcnt(0)
	s_barrier
	s_load_dwordx4 s[12:15], s[24:25], 0xe8
	v_bitop3_b32 v202, v186, v5, 32 bitop3:0x36
	v_bitop3_b32 v203, v186, v5, 64 bitop3:0x36
	v_bitop3_b32 v207, v186, v5, s21 bitop3:0x36
	v_bitop3_b32 v213, v186, v5, s4 bitop3:0x36
	s_load_dwordx2 s[20:21], s[24:25], 0xa0
	s_load_dwordx2 s[22:23], s[24:25], 0xb0
	v_mad_i64_i32 v[4:5], s[24:25], s16, v4, v[70:71]
	v_lshlrev_b32_e32 v66, 4, v6
	s_add_u32 s6, s6, s27
	v_lshl_add_u64 v[4:5], v[4:5], 0, v[66:67]
	s_addc_u32 s7, s7, s26
	v_lshl_add_u64 v[4:5], s[8:9], 0, v[4:5]
	s_mov_b64 s[8:9], 0xa000
	v_lshl_add_u64 v[2:3], s[6:7], 0, v[2:3]
	s_mov_b64 s[6:7], 0x10000
	v_mov_b32_e32 v66, v67
	v_cvt_pk_bf16_f32 v135, v52, v53
	v_cvt_pk_bf16_f32 v140, v50, v51
	v_cvt_pk_bf16_f32 v142, v38, v39
	v_lshl_add_u64 v[188:189], v[4:5], 0, s[8:9]
	v_lshl_add_u64 v[190:191], v[2:3], 0, s[6:7]
	v_mov_b32_e32 v68, v67
	v_mov_b32_e32 v69, v67
	v_mov_b32_e32 v70, v67
	v_mov_b32_e32 v71, v67
	v_mov_b32_e32 v72, v67
	v_mov_b32_e32 v73, v67
	v_mov_b32_e32 v74, v67
	v_mov_b32_e32 v75, v67
	v_mov_b32_e32 v76, v67
	v_mov_b32_e32 v77, v67
	v_mov_b32_e32 v78, v67
	v_mov_b32_e32 v79, v67
	v_mov_b32_e32 v80, v67
	v_mov_b32_e32 v81, v67
	v_mov_b64_e32 v[50:51], v[66:67]
	v_mov_b64_e32 v[34:35], v[66:67]
	v_mov_b64_e32 v[18:19], v[66:67]
	v_mov_b64_e32 v[2:3], v[66:67]
	v_cvt_pk_bf16_f32 v132, v84, v85
	v_lshlrev_b32_e32 v200, 9, v192
	v_cmp_gt_u32_e64 s[4:5], 32, v187
	v_lshl_add_u32 v210, v192, 2, v185
	v_mov_b32_e32 v215, 0xf149f2ca
	s_mov_b32 s35, -2
	s_movk_i32 s30, 0x84
	s_movk_i32 s31, 0x7ff
	s_mov_b32 s34, 0x42ddb3d8
	s_mov_b64 s[8:9], 0x4000
	s_mov_b64 s[24:25], 0x6000
	v_mov_b32_e32 v216, 0xfffff800
	v_mov_b32_e32 v217, 0x80
	v_mov_b64_e32 v[52:53], v[68:69]
	v_mov_b64_e32 v[54:55], v[70:71]
	v_mov_b64_e32 v[56:57], v[72:73]
	v_mov_b64_e32 v[58:59], v[74:75]
	v_mov_b64_e32 v[60:61], v[76:77]
	v_mov_b64_e32 v[62:63], v[78:79]
	v_mov_b64_e32 v[64:65], v[80:81]
	v_mov_b64_e32 v[36:37], v[68:69]
	v_mov_b64_e32 v[38:39], v[70:71]
	v_mov_b64_e32 v[40:41], v[72:73]
	v_mov_b64_e32 v[42:43], v[74:75]
	v_mov_b64_e32 v[44:45], v[76:77]
	v_mov_b64_e32 v[46:47], v[78:79]
	v_mov_b64_e32 v[48:49], v[80:81]
	v_mov_b64_e32 v[20:21], v[68:69]
	v_mov_b64_e32 v[22:23], v[70:71]
	v_mov_b64_e32 v[24:25], v[72:73]
	v_mov_b64_e32 v[26:27], v[74:75]
	v_mov_b64_e32 v[28:29], v[76:77]
	v_mov_b64_e32 v[30:31], v[78:79]
	v_mov_b64_e32 v[32:33], v[80:81]
	v_mov_b64_e32 v[4:5], v[68:69]
	v_mov_b64_e32 v[6:7], v[70:71]
	v_mov_b64_e32 v[8:9], v[72:73]
	v_mov_b64_e32 v[10:11], v[74:75]
	v_mov_b64_e32 v[12:13], v[76:77]
	v_mov_b64_e32 v[14:15], v[78:79]
	v_mov_b64_e32 v[16:17], v[80:81]
	v_mov_b32_e32 v218, 0
	s_waitcnt lgkmcnt(0)
	s_lshr_b32 s56, s2, 1
	s_and_b32 s57, s56, 31
	s_lshl_b32 s57, s57, 7
	s_or_b32 s57, s57, s53
	s_lshr_b32 s58, s56, 5
	s_lshl_b32 s58, s58, 7
	s_and_b32 s59, s56, 15
	s_lshl_b32 s59, s59, 7
	s_or_b32 s59, s59, s53
	s_lshr_b32 s60, s56, 4
	s_lshl_b32 s60, s60, 7
	v_lshrrev_b32_e32 v253, 3, v0
	v_and_b32_e32 v254, 7, v0
	v_lshlrev_b32_e32 v254, 4, v254
	v_mul_u32_u24_e32 v244, 0x84, v253
	v_add_u32_e32 v244, v244, v254
	v_add_u32_e32 v244, 0x20800, v244
	v_and_b32_e32 v255, 15, v0
	v_mul_u32_u24_e32 v245, 0x210, v255
	v_lshrrev_b32_e32 v252, 4, v0
	v_lshl_add_u32 v245, v252, 2, v245
	v_add_u32_e32 v245, 0x20800, v245
	v_add_u32_e32 v246, s57, v253
	v_and_b32_e32 v247, 0x7ff, v246
	v_lshrrev_b32_e32 v246, 11, v246
	v_lshlrev_b32_e32 v246, 7, v246
	v_and_b32_e32 v251, 0x7f, v247
	v_or_b32_e32 v246, v246, v251
	v_lshrrev_b32_e32 v247, 7, v247
	v_lshl_or_b32 v246, v247, 8, v246
	v_lshlrev_b32_e32 v246, 11, v246
	v_add_u32_e32 v246, v246, v254
	v_add_u32_e32 v246, s58, v246
	v_add_u32_e32 v247, s59, v253
	v_lshlrev_b32_e32 v247, 11, v247
	v_add_u32_e32 v247, v247, v254
	v_add_u32_e32 v247, s60, v247
	v_lshlrev_b32_e32 v251, 2, v252
	v_lshlrev_b32_e32 v255, 2, v255
	v_add_u32_e32 v248, s58, v251
	v_lshlrev_b32_e32 v248, 14, v248
	v_add_u32_e32 v249, s57, v255
	v_lshl_add_u32 v248, v249, 2, v248
	v_add_u32_e32 v252, s60, v251
	v_lshlrev_b32_e32 v252, 13, v252
	v_add_u32_e32 v249, s59, v255
	v_lshl_add_u32 v252, v249, 2, v252
	v_mov_b32_e32 v248, v252
	v_add_u32_e32 v249, 0x2000, v252
	v_add_u32_e32 v250, 0x4000, v252
	v_add_u32_e32 v251, 0x6000, v252
	s_add_u32 s62, s22, 0x1800000
	s_addc_u32 s63, s23, 0
	s_add_i32 s38, s35, 2
	s_and_b32 s37, s38, 1
	s_cmpk_eq_i32 s35, 0x41
	s_cbranch_scc0 .LBB0_1100

; DEV int ltid() { int t = threadIdx.x; asm volatile("" : "+v"(t)); return t; }
; DEV void fill_store(CParams& p, int wg, int slot, int bufsel) {
;   extern __shared__ __attribute__((aligned(16))) char shm[];
;   const unsigned* T = (const unsigned*)(shm + FILL_LDS_OFF + bufsel * FILL_TB); const int tid = ltid(), nl = tid >> 3, cc = tid & 7;
;   const FillDesc d = fill_decode(p, wg, slot);
;   u32x4 v; v.x = T[nl * 33 + 4 * cc]; v.y = T[nl * 33 + 4 * cc + 1]; v.z = T[nl * 33 + 4 * cc + 2]; v.w = T[nl * 33 + 4 * cc + 3];
;   *(u32x4*)(d.dst + (long)perm_row(d.perm, d.n0 + nl) * 2048 + d.kh + 16 * cc) = v;
; }
.LBB0_1106:
	s_xor_b32 s56, s37, 1
	s_mul_i32 s56, s56, 0x2200
	v_add_u32_e32 v72, s56, v244
	ds_read2_b32 v[68:69], v72 offset1:1
	ds_read2_b32 v[70:71], v72 offset0:2 offset1:3
	s_add_i32 s57, s38, 129
	s_sub_u32 s57, s57, 0x80
	s_lshr_b32 s58, s57, 1
	s_lshl_b32 s58, s58, 22
	s_and_b32 s59, s57, 1
	s_lshl_b32 s59, s59, 10
	s_or_b32 s58, s58, s59
	s_add_u32 s60, s14, s58
	s_addc_u32 s61, s15, 0
	s_waitcnt lgkmcnt(0)
	global_store_dwordx4 v247, v[68:71], s[60:61]

; DEV void finishSM(f32x16& p0, f32x16& p1, float alpha, float& l_reg, bf16x8& pa0, bf16x8& pa1, bf16x8& pa2, bf16x8& pa3) {
; #pragma unroll
;   for (int r = 0; r < 16; ++r) p1[r] = __builtin_amdgcn_exp2f(p1[r]);
;   float ps = 0;
; #pragma unroll
;   for (int r = 0; r < 16; ++r) ps += p0[r];
; #pragma unroll
;   for (int r = 0; r < 16; ++r) ps += p1[r];
;   { auto rr = __builtin_amdgcn_permlane32_swap(__float_as_uint(ps), __float_as_uint(ps), false, false);
;     ps = __uint_as_float(rr[0]) + __uint_as_float(rr[1]); }
;   l_reg = l_reg * alpha + ps;
;     ...
;   PK4(p0, 0, pa0); PK4(p0, 8, pa1); PK4(p1, 0, pa2); PK4(p1, 8, pa3);
;     ...
; }
; DEV void qkt(f32x16& p0, f32x16& p1, const char* Ks, const bf16x8* qr, int r32, int hi) {
;   p0 = f32x16{}; p1 = f32x16{};
;   __builtin_amdgcn_s_setprio(1);
; #pragma unroll
;   for (int d0 = 0; d0 < 12; ++d0) { const int cb = (d0 * 16 + hi * 8) * 2;
;     const bf16x8 b0 = *reinterpret_cast<const bf16x8*>(Ks + KSWZ2(r32, cb));
;     const bf16x8 b1 = *reinterpret_cast<const bf16x8*>(Ks + KSWZ2(32 + r32, cb));
;     p0 = __builtin_amdgcn_mfma_f32_32x32x16_bf16(b0, qr[d0], p0, 0, 0, 0);
;     p1 = __builtin_amdgcn_mfma_f32_32x32x16_bf16(b1, qr[d0], p1, 0, 0, 0); }
;   __builtin_amdgcn_s_setprio(0);
; }
; DEV int v_st(int k, int c) { const int kk = (k & ~0xC) | ((k & 4) << 1) | ((k & 8) >> 1); return ((kk >> 3) * 4 + (c >> 5)) * 512 + ((kk & 7) * 32 + (c & 31)) * 2; }
; DEV int v_rd_base(int lane) { return ((lane & 3) << 3) | (((lane >> 2) & 3) << 6) | (((lane >> 4) & 1) << 5) | (((lane >> 5) & 1) << 8); }
; template <int OFF> DEV s16x4 tr_read(int vb) { s16x4 r; asm volatile("ds_read_b64_tr_b16 %0, %1 offset:%2" : "=&v"(r) : "v"(vb), "i"(OFF) : "memory"); return r; }
; template <int D0> DEV void pv_read(VFrag& f, int vb) {
;   f.l0 = tr_read<v_rd_off(D0, 0, 0)>(vb); f.h0 = tr_read<v_rd_off(D0, 0, 1)>(vb); f.l1 = tr_read<v_rd_off(D0, 1, 0)>(vb); f.h1 = tr_read<v_rd_off(D0, 1, 1)>(vb);
;   f.l2 = tr_read<v_rd_off(D0, 2, 0)>(vb); f.h2 = tr_read<v_rd_off(D0, 2, 1)>(vb); f.l3 = tr_read<v_rd_off(D0, 3, 0)>(vb); f.h3 = tr_read<v_rd_off(D0, 3, 1)>(vb);
; }
; DEV void pv_mma(f32x16& od, const VFrag& f, bf16x8 pa0, bf16x8 pa1, bf16x8 pa2, bf16x8 pa3) {
;     ...
;   __builtin_amdgcn_s_setprio(1);
;   od = __builtin_amdgcn_mfma_f32_32x32x16_bf16(pa0, PK(f.l0, f.h0), od, 0, 0, 0);
.LBB0_1118:
	v_cndmask_b32_e64 v215, v66, v215, s[6:7]
	v_mul_f32_e32 v66, 0xbdd53b94, v215
	v_fmamk_f32 v84, v84, 0x3dd53b94, v66
	v_fmamk_f32 v85, v85, 0x3dd53b94, v66
	v_fmamk_f32 v86, v86, 0x3dd53b94, v66
	v_fmamk_f32 v87, v87, 0x3dd53b94, v66
	v_fmamk_f32 v88, v88, 0x3dd53b94, v66
	v_fmamk_f32 v89, v89, 0x3dd53b94, v66
	v_fmamk_f32 v90, v90, 0x3dd53b94, v66
	v_fmamk_f32 v91, v91, 0x3dd53b94, v66
	v_fmamk_f32 v92, v92, 0x3dd53b94, v66
	v_fmamk_f32 v93, v93, 0x3dd53b94, v66
	v_fmamk_f32 v94, v94, 0x3dd53b94, v66
	v_fmamk_f32 v95, v95, 0x3dd53b94, v66
	v_fmamk_f32 v96, v96, 0x3dd53b94, v66
	v_fmamk_f32 v97, v97, 0x3dd53b94, v66
	v_fmamk_f32 v98, v98, 0x3dd53b94, v66
	v_fmamk_f32 v99, v99, 0x3dd53b94, v66
	v_fmamk_f32 v68, v68, 0x3dd53b94, v66
	v_fmamk_f32 v69, v69, 0x3dd53b94, v66
	v_fmamk_f32 v70, v70, 0x3dd53b94, v66
	v_fmamk_f32 v71, v71, 0x3dd53b94, v66
	v_fmamk_f32 v72, v72, 0x3dd53b94, v66
	v_fmamk_f32 v73, v73, 0x3dd53b94, v66
	v_fmamk_f32 v74, v74, 0x3dd53b94, v66
	v_fmamk_f32 v75, v75, 0x3dd53b94, v66
	v_fmamk_f32 v76, v76, 0x3dd53b94, v66
	v_fmamk_f32 v77, v77, 0x3dd53b94, v66
	v_fmamk_f32 v78, v78, 0x3dd53b94, v66
	v_fmamk_f32 v79, v79, 0x3dd53b94, v66
	v_fmamk_f32 v80, v80, 0x3dd53b94, v66
	v_fmamk_f32 v81, v81, 0x3dd53b94, v66
	v_fmamk_f32 v82, v82, 0x3dd53b94, v66
	v_fmac_f32_e32 v66, 0x3dd53b94, v83
	v_exp_f32_e32 v83, v84
	v_exp_f32_e32 v84, v85
	v_exp_f32_e32 v85, v86
	v_exp_f32_e32 v86, v87
	v_exp_f32_e32 v87, v88
	v_exp_f32_e32 v88, v89
	v_exp_f32_e32 v89, v90
	v_exp_f32_e32 v90, v91
	v_exp_f32_e32 v91, v92
	v_exp_f32_e32 v92, v93
	v_exp_f32_e32 v93, v94
	v_exp_f32_e32 v94, v95
	v_exp_f32_e32 v95, v96
	v_exp_f32_e32 v96, v97
	v_exp_f32_e32 v97, v98
	v_exp_f32_e32 v98, v99
	v_exp_f32_e32 v99, v68
	v_add_f32_e32 v68, 0, v83
	v_add_f32_e32 v68, v84, v68
	v_add_f32_e32 v68, v85, v68
	v_add_f32_e32 v68, v86, v68
	v_add_f32_e32 v68, v87, v68
	v_add_f32_e32 v68, v88, v68
	v_add_f32_e32 v68, v89, v68
	v_add_f32_e32 v68, v90, v68
	v_add_f32_e32 v68, v91, v68
	v_add_f32_e32 v68, v92, v68
	v_add_f32_e32 v68, v93, v68
	v_add_f32_e32 v68, v94, v68
	v_add_f32_e32 v68, v95, v68
	v_exp_f32_e32 v220, v69
	v_add_f32_e32 v68, v96, v68
	v_exp_f32_e32 v221, v70
	v_add_f32_e32 v68, v97, v68
	v_exp_f32_e32 v222, v71
	v_add_f32_e32 v68, v98, v68
	v_exp_f32_e32 v224, v72
	v_add_f32_e32 v68, v99, v68
	v_exp_f32_e32 v225, v73
	v_add_f32_e32 v68, v220, v68
	v_exp_f32_e32 v226, v74
	v_add_f32_e32 v68, v221, v68
	v_exp_f32_e32 v227, v75
	v_add_f32_e32 v68, v222, v68
	v_exp_f32_e32 v228, v76
	v_add_f32_e32 v68, v224, v68
	v_exp_f32_e32 v229, v77
	v_add_f32_e32 v68, v225, v68
	v_exp_f32_e32 v230, v78
	v_add_f32_e32 v68, v226, v68
	v_exp_f32_e32 v231, v79
	v_add_f32_e32 v68, v227, v68
	v_exp_f32_e32 v232, v80
	v_add_f32_e32 v68, v228, v68
	v_exp_f32_e32 v233, v81
	v_add_f32_e32 v68, v229, v68
	v_exp_f32_e32 v234, v82
	v_add_f32_e32 v68, v230, v68
	v_exp_f32_e32 v66, v66
	v_add_f32_e32 v68, v231, v68
	v_add_f32_e32 v68, v232, v68
	v_add_f32_e32 v68, v233, v68
	v_add_f32_e32 v68, v234, v68
	v_add_f32_e32 v68, v66, v68
	v_mov_b32_e32 v69, v68
	s_nop 1
	v_permlane32_swap_b32_e32 v68, v69
	v_cvt_pk_bf16_f32 v70, v83, v84
	v_cvt_pk_bf16_f32 v71, v85, v86
	v_cvt_pk_bf16_f32 v72, v87, v88
	v_cvt_pk_bf16_f32 v73, v89, v90
	v_cvt_pk_bf16_f32 v74, v91, v92
	v_cvt_pk_bf16_f32 v75, v93, v94
	v_cvt_pk_bf16_f32 v76, v95, v96
	v_cvt_pk_bf16_f32 v77, v97, v98
	v_cvt_pk_bf16_f32 v78, v99, v220
	v_cvt_pk_bf16_f32 v79, v221, v222
	v_cvt_pk_bf16_f32 v80, v224, v225
	v_cvt_pk_bf16_f32 v81, v226, v227
	v_cvt_pk_bf16_f32 v82, v228, v229
	v_cvt_pk_bf16_f32 v83, v230, v231
	v_cvt_pk_bf16_f32 v84, v232, v233
	v_cvt_pk_bf16_f32 v85, v234, v66
	v_permlane32_swap_b32_e32 v70, v72
	v_permlane32_swap_b32_e32 v71, v73
	v_permlane32_swap_b32_e32 v74, v76
	v_permlane32_swap_b32_e32 v75, v77
	v_permlane32_swap_b32_e32 v78, v80
	v_permlane32_swap_b32_e32 v79, v81
	v_permlane32_swap_b32_e32 v82, v84
	v_permlane32_swap_b32_e32 v83, v85
	v_lshl_add_u32 v66, s37, 14, v214
	ds_read_b64_tr_b16 v[86:87], v66 offset:0
	ds_read_b64_tr_b16 v[88:89], v66 offset:0x800
	ds_read_b64_tr_b16 v[90:91], v66 offset:0x1000
	ds_read_b64_tr_b16 v[92:93], v66 offset:0x1800
	ds_read_b64_tr_b16 v[94:95], v66 offset:0x2000
	ds_read_b64_tr_b16 v[96:97], v66 offset:0x2800
	ds_read_b64_tr_b16 v[224:225], v66 offset:0x3000
	ds_read_b64_tr_b16 v[226:227], v66 offset:0x3800
	ds_read_b64_tr_b16 v[228:229], v66 offset:0x200
	ds_read_b64_tr_b16 v[230:231], v66 offset:0xa00
	ds_read_b64_tr_b16 v[232:233], v66 offset:0x1200
	ds_read_b64_tr_b16 v[234:235], v66 offset:0x1a00
	ds_read_b64_tr_b16 v[236:237], v66 offset:0x2200
	ds_read_b64_tr_b16 v[238:239], v66 offset:0x2a00
	ds_read_b64_tr_b16 v[240:241], v66 offset:0x3200
	ds_read_b64_tr_b16 v[242:243], v66 offset:0x3a00
	s_waitcnt lgkmcnt(8)
	s_setprio 1
	v_mfma_f32_32x32x16_bf16 v[50:65], v[70:73], v[86:89], v[50:65]
	v_mfma_f32_32x32x16_bf16 v[50:65], v[74:77], v[90:93], v[50:65]
	v_mfma_f32_32x32x16_bf16 v[50:65], v[78:81], v[94:97], v[50:65]
	v_mfma_f32_32x32x16_bf16 v[50:65], v[82:85], v[224:227], v[50:65]
	s_setprio 0
	ds_read_b64_tr_b16 v[86:87], v66 offset:0x400
	ds_read_b64_tr_b16 v[88:89], v66 offset:0xc00
	ds_read_b64_tr_b16 v[90:91], v66 offset:0x1400
	ds_read_b64_tr_b16 v[92:93], v66 offset:0x1c00
	ds_read_b64_tr_b16 v[94:95], v66 offset:0x2400
	ds_read_b64_tr_b16 v[96:97], v66 offset:0x2c00
	ds_read_b64_tr_b16 v[224:225], v66 offset:0x3400
	ds_read_b64_tr_b16 v[226:227], v66 offset:0x3c00
	s_waitcnt lgkmcnt(8)
	s_setprio 1
	v_mfma_f32_32x32x16_bf16 v[34:49], v[70:73], v[228:231], v[34:49]
	v_mfma_f32_32x32x16_bf16 v[34:49], v[74:77], v[232:235], v[34:49]
	v_mfma_f32_32x32x16_bf16 v[34:49], v[78:81], v[236:239], v[34:49]
	v_mfma_f32_32x32x16_bf16 v[34:49], v[82:85], v[240:243], v[34:49]
	s_setprio 0
	ds_read_b64_tr_b16 v[228:229], v66 offset:0x600
	ds_read_b64_tr_b16 v[230:231], v66 offset:0xe00
	ds_read_b64_tr_b16 v[232:233], v66 offset:0x1600
	ds_read_b64_tr_b16 v[234:235], v66 offset:0x1e00
	ds_read_b64_tr_b16 v[236:237], v66 offset:0x2600
	ds_read_b64_tr_b16 v[238:239], v66 offset:0x2e00
	ds_read_b64_tr_b16 v[240:241], v66 offset:0x3600
	ds_read_b64_tr_b16 v[242:243], v66 offset:0x3e00
	s_waitcnt lgkmcnt(8)
	s_setprio 1
	v_mfma_f32_32x32x16_bf16 v[18:33], v[70:73], v[86:89], v[18:33]
	v_mfma_f32_32x32x16_bf16 v[18:33], v[74:77], v[90:93], v[18:33]
	v_mfma_f32_32x32x16_bf16 v[18:33], v[78:81], v[94:97], v[18:33]
	v_mfma_f32_32x32x16_bf16 v[18:33], v[82:85], v[224:227], v[18:33]
	s_setprio 0
	s_waitcnt lgkmcnt(0)
	s_setprio 1
	v_mfma_f32_32x32x16_bf16 v[2:17], v[70:73], v[228:231], v[2:17]
	v_mfma_f32_32x32x16_bf16 v[2:17], v[74:77], v[232:235], v[2:17]
	v_mfma_f32_32x32x16_bf16 v[2:17], v[78:81], v[236:239], v[2:17]
	v_mfma_f32_32x32x16_bf16 v[2:17], v[82:85], v[240:243], v[2:17]
	s_setprio 0
	s_cmp_gt_u32 s38, 61
	s_cbranch_scc1 .LBB0_1126
; DEV int ltid() { int t = threadIdx.x; asm volatile("" : "+v"(t)); return t; }
; DEV unsigned cvt_pk4_fp8(f32x4 v) { unsigned r = 0; r = __builtin_amdgcn_cvt_pk_fp8_f32(v[0], v[1], r, false); r = __builtin_amdgcn_cvt_pk_fp8_f32(v[2], v[3], r, true); return r; }
; DEV void fill_load(CParams& p, int wg, int slot, f32x4 (&ld)[4]) {
;   const FillDesc d = fill_decode(p, wg, slot); const int tid = ltid(), tx = tid & 15, ty = tid >> 4;
;   const float* sp = d.src + (long)(d.kh + 4 * ty) * d.ldsrc + d.n0 + 4 * tx;
; #pragma unroll
;   for (int r = 0; r < 4; ++r) ld[r] = *(const f32x4*)(sp + (long)r * d.ldsrc);
; }
; DEV void fill_write(const f32x4 (&ld)[4], int bufsel) {
;   extern __shared__ __attribute__((aligned(16))) char shm[];
;   unsigned* T = (unsigned*)(shm + FILL_LDS_OFF + bufsel * FILL_TB); const int tid = ltid(), tx = tid & 15, ty = tid >> 4;
;   constexpr float WS = (float)(1 << FP8_WSCALE_LOG2_);
; #pragma unroll
;   for (int j = 0; j < 4; ++j) T[(4 * tx + j) * 33 + ty] = cvt_pk4_fp8((f32x4){ld[0][j] * WS, ld[1][j] * WS, ld[2][j] * WS, ld[3][j] * WS});
; }
	s_waitcnt vmcnt(3)
	v_mul_f32_e32 v71, 0x42800000, v168
	s_waitcnt vmcnt(2)
	v_mul_f32_e32 v72, 0x42800000, v172
	v_cvt_pk_fp8_f32 v73, v71, v72
	s_waitcnt vmcnt(1)
	v_mul_f32_e32 v71, 0x42800000, v176
	s_waitcnt vmcnt(0)
	v_mul_f32_e32 v72, 0x42800000, v180
	v_cvt_pk_fp8_f32 v73, v71, v72 op_sel:[0,0,1]
	v_mul_f32_e32 v71, 0x42800000, v169
	v_mul_f32_e32 v72, 0x42800000, v173
	v_cvt_pk_fp8_f32 v74, v71, v72
	v_mul_f32_e32 v71, 0x42800000, v177
	v_mul_f32_e32 v72, 0x42800000, v181
	v_cvt_pk_fp8_f32 v74, v71, v72 op_sel:[0,0,1]
	v_mul_f32_e32 v71, 0x42800000, v170
	v_mul_f32_e32 v72, 0x42800000, v174
	v_cvt_pk_fp8_f32 v77, v71, v72
	v_mul_f32_e32 v71, 0x42800000, v171
	v_mul_f32_e32 v72, 0x42800000, v175
	v_cvt_pk_fp8_f32 v78, v71, v72
	v_mul_f32_e32 v75, 0x42800000, v178
	v_mul_f32_e32 v76, 0x42800000, v182
	v_mul_f32_e32 v71, 0x42800000, v179
	v_mul_f32_e32 v72, 0x42800000, v183
	v_cvt_pk_fp8_f32 v77, v75, v76 op_sel:[0,0,1]
	v_cvt_pk_fp8_f32 v78, v71, v72 op_sel:[0,0,1]
	s_mul_i32 s56, s37, 0x2200
	s_cmp_eq_u32 s35, 59
	v_add_u32_e32 v66, s56, v245
	ds_write2_b32 v66, v73, v74 offset1:33
	ds_write2_b32 v66, v77, v78 offset0:66 offset1:99
	s_cbranch_scc1 .LBB0_1126
	global_load_dwordx4 v[168:171], v248, s[62:63]
	global_load_dwordx4 v[172:175], v249, s[62:63]
	global_load_dwordx4 v[176:179], v250, s[62:63]
	global_load_dwordx4 v[180:183], v251, s[62:63]
	s_add_u32 s62, s62, 0x800000
	s_addc_u32 s63, s63, 0
